# GEMM phases: first K-trip after an epilogue no longer waits for the epilogue stores (counted vmcnt), phase prologue drains instead
# speedup vs baseline: 1.0016x; 1.0016x over previous
; #define PG8_STAGE(bufoff, gbase, voff) do { const char* gb_ = (const char*)(gbase); asm volatile("" : "+s"(gb_));     \
;         _Pragma("unroll") for (int _i = 0; _i < 2; ++_i) \
;         __builtin_amdgcn_global_load_lds((const unsigned*)(gb_ + (voff)[_i]), (LAS unsigned*)(lds + (bufoff) + ldsw + _i * 8192), 16, 0, 0); } while (0)
; #define PG8_STAGE_A(bufoff, gbase, h, vo) do { if constexpr (GATHER) { PG8_STAGE(bufoff, gbase, (vo)[h]); } else { PG8_STAGE(bufoff, (gbase) + (h) * hstep, voffA); } } while (0)
; #define PG8_WAIT_V(n) asm volatile("s_waitcnt vmcnt(" #n ")" ::: "memory")
; #define PG8_BAR __builtin_amdgcn_s_barrier()
;     ...
;     if constexpr (SP2) {
;         PG8_STAGE(PG8_SB(0, 0), cB + PG8_KO(0), voffB); PG8_STAGE(PG8_SB(0, 1), cB + hstep + PG8_KO(0), voffB); PG8_STAGE_A(PG8_SA(0, 0), cA + PG8_KO(0), 0, cvo); PG8_STAGE_A(PG8_SA(0, 1), cA + PG8_KO(0), 1, cvo);
;         if (wr == 1) PG8_BAR;
;         PG8_WAIT_V(2); PG8_BAR;
;         PG8_STAGE(PG8_SB(1, 0), cB + PG8_KO(1), voffB); PG8_STAGE_A(PG8_SA(1, 0), cA + PG8_KO(1), 0, cvo); PG8_STAGE(PG8_SB(1, 1), cB + hstep + PG8_KO(1), voffB);
;         PG8_WAIT_V(6); PG8_BAR;
.LBB0_464:
	v_lshrrev_b32_e32 v4, 1, v2
	v_and_b32_e32 v4, 24, v4
	v_and_b32_e32 v3, 15, v2
	v_lshlrev_b32_e32 v5, 1, v4
	v_lshlrev_b32_e32 v2, 2, v2
	s_lshl_b32 s3, s3, 5
	v_lshl_or_b32 v1, s4, 6, v3
	v_lshl_or_b32 v3, v3, 6, v5
	s_lshl_b32 s4, s4, 13
	v_and_b32_e32 v2, 32, v2
	s_and_b32 s3, s3, 0x60
	v_bitop3_b32 v5, v3, s4, v2 bitop3:0xde
	s_lshl_b32 s4, s3, 7
	v_bitop3_b32 v146, v3, s4, v2 bitop3:0xde
	s_add_u32 s4, s30, 0x80
	v_mov_b32_e32 v133, v191
	s_addc_u32 s5, s31, 0
	s_waitcnt vmcnt(2)
	s_barrier
	s_add_i32 m0, s23, 0x18000
	v_lshl_add_u64 v[2:3], s[4:5], 0, v[132:133]
	v_mov_b32_e32 v131, v191
	global_load_lds_dwordx4 v[2:3], off
	s_add_i32 m0, s23, 0x1a000
	v_lshl_add_u64 v[2:3], s[4:5], 0, v[130:131]
	s_add_u32 s4, s34, 0x80
	s_addc_u32 s5, s35, 0
	s_add_i32 s57, s23, 0x8000
	global_load_lds_dwordx4 v[2:3], off
	s_mov_b32 m0, s57
	v_lshl_add_u64 v[2:3], s[4:5], 0, v[132:133]
	s_add_i32 s58, s23, 0xa000
	global_load_lds_dwordx4 v[2:3], off
	v_lshl_add_u64 v[2:3], s[4:5], 0, v[130:131]
	s_add_u32 s4, s30, 0x40080
	s_mov_b32 m0, s58
	s_addc_u32 s5, s31, 0
	global_load_lds_dwordx4 v[2:3], off
	s_add_i32 m0, s23, 0x1c000
	v_lshl_add_u64 v[2:3], s[4:5], 0, v[132:133]
	global_load_lds_dwordx4 v[2:3], off
	v_lshl_add_u64 v[2:3], s[4:5], 0, v[130:131]
	s_add_i32 m0, s23, 0x1e000
	v_or_b32_e32 v147, s3, v4
	global_load_lds_dwordx4 v[2:3], off
	s_waitcnt vmcnt(0)
	s_cmpk_lt_u32 s2, 0x100
	v_or_b32_e32 v148, 0xfffffe00, v147
	s_cselect_b64 s[2:3], -1, 0
	s_mov_b32 s59, 0
	v_add_u32_e32 v149, 0, v5
	s_barrier
	s_branch .LBB0_467

;     ...
;         PG8_TRIP(0, true);
.LBB0_469:
	s_ashr_i32 s7, s6, 31
	s_lshl_b64 s[8:9], s[6:7], 19
	s_add_u32 s8, s96, s8
	s_addc_u32 s9, s97, s9
	s_ashr_i32 s5, s4, 31
	s_lshl_b64 s[10:11], s[4:5], 19
	s_add_u32 s10, s17, s10
	s_addc_u32 s11, s25, s11
	s_add_u32 s18, s34, 0x100
	s_addc_u32 s19, s35, 0
	s_add_u32 s42, s34, 0x180
	s_addc_u32 s43, s35, 0
	s_add_u32 s46, s30, 0x100
	s_addc_u32 s47, s31, 0
	s_add_i32 s61, 0, 0x10000
	s_add_i32 s52, 0, 0x14000
	v_add_u32_e32 v134, s61, v146
	v_add_u32_e32 v135, s52, v146
	ds_read_b128 v[2:5], v134
	ds_read_b128 v[6:9], v134 offset:1024
	ds_read_b128 v[10:13], v134 offset:2048
	ds_read_b128 v[14:17], v134 offset:3072
	ds_read_b128 v[18:21], v135
	ds_read_b128 v[22:25], v135 offset:1024
	ds_read_b128 v[26:29], v135 offset:2048
	ds_read_b128 v[30:33], v135 offset:3072
	s_mov_b64 s[40:41], 0x100
	s_add_u32 s50, s34, 0x40080
	s_addc_u32 s51, s35, 0
	s_add_i32 s5, s23, 0xc000
	ds_read_b128 v[34:37], v149
	ds_read_b128 v[38:41], v149 offset:1024
	ds_read_b128 v[42:45], v149 offset:2048
	ds_read_b128 v[46:49], v149 offset:3072
	ds_read_b128 v[50:53], v149 offset:4096
	ds_read_b128 v[54:57], v149 offset:5120
	ds_read_b128 v[58:61], v149 offset:6144
	ds_read_b128 v[62:65], v149 offset:7168
	s_mov_b32 m0, s5
	v_lshl_add_u64 v[66:67], s[50:51], 0, v[132:133]
	s_add_i32 s7, s23, 0xe000
	global_load_lds_dwordx4 v[66:67], off
	v_lshl_add_u64 v[66:67], s[50:51], 0, v[130:131]
	s_mov_b32 m0, s7
	s_nop 0
	global_load_lds_dwordx4 v[66:67], off
	s_waitcnt vmcnt(16)
	s_waitcnt lgkmcnt(0)
	s_barrier
	s_setprio 1
	s_waitcnt lgkmcnt(0)
	v_mfma_f32_16x16x32_bf16 v[86:89], v[10:13], v[50:53], 0
	v_mfma_f32_16x16x32_bf16 v[90:93], v[14:17], v[54:57], v[86:89]
	v_mfma_f32_16x16x32_bf16 v[86:89], v[2:5], v[58:61], 0
	v_mfma_f32_16x16x32_bf16 v[66:69], v[2:5], v[34:37], 0
	v_mfma_f32_16x16x32_bf16 v[70:73], v[10:13], v[34:37], 0
	v_mfma_f32_16x16x32_bf16 v[74:77], v[2:5], v[42:45], 0
	v_mfma_f32_16x16x32_bf16 v[78:81], v[10:13], v[42:45], 0
	v_mfma_f32_16x16x32_bf16 v[82:85], v[2:5], v[50:53], 0
	v_mfma_f32_16x16x32_bf16 v[94:97], v[6:9], v[62:65], v[86:89]
	v_mfma_f32_16x16x32_bf16 v[86:89], v[10:13], v[58:61], 0
	v_mfma_f32_16x16x32_bf16 v[66:69], v[6:9], v[38:41], v[66:69]
	v_mfma_f32_16x16x32_bf16 v[70:73], v[14:17], v[38:41], v[70:73]
	v_mfma_f32_16x16x32_bf16 v[74:77], v[6:9], v[46:49], v[74:77]
	v_mfma_f32_16x16x32_bf16 v[78:81], v[14:17], v[46:49], v[78:81]
	v_mfma_f32_16x16x32_bf16 v[82:85], v[6:9], v[54:57], v[82:85]
	v_mfma_f32_16x16x32_bf16 v[102:105], v[14:17], v[62:65], v[86:89]
	s_setprio 0
	s_setprio 1
	v_mfma_f32_16x16x32_bf16 v[86:89], v[18:21], v[34:37], 0
	v_mfma_f32_16x16x32_bf16 v[34:37], v[26:29], v[34:37], 0
	v_mfma_f32_16x16x32_bf16 v[110:113], v[22:25], v[38:41], v[86:89]
	v_mfma_f32_16x16x32_bf16 v[34:37], v[30:33], v[38:41], v[34:37]
	v_mfma_f32_16x16x32_bf16 v[38:41], v[18:21], v[42:45], 0
	v_mfma_f32_16x16x32_bf16 v[138:141], v[22:25], v[46:49], v[38:41]
	v_mfma_f32_16x16x32_bf16 v[38:41], v[26:29], v[42:45], 0
	v_mfma_f32_16x16x32_bf16 v[42:45], v[30:33], v[46:49], v[38:41]
	v_mfma_f32_16x16x32_bf16 v[38:41], v[18:21], v[50:53], 0
	v_mfma_f32_16x16x32_bf16 v[46:49], v[22:25], v[54:57], v[38:41]
	v_mfma_f32_16x16x32_bf16 v[38:41], v[26:29], v[50:53], 0
	v_mfma_f32_16x16x32_bf16 v[50:53], v[30:33], v[54:57], v[38:41]
	v_mfma_f32_16x16x32_bf16 v[38:41], v[18:21], v[58:61], 0
	v_mfma_f32_16x16x32_bf16 v[142:145], v[22:25], v[62:65], v[38:41]
	v_mfma_f32_16x16x32_bf16 v[38:41], v[26:29], v[58:61], 0
	v_mfma_f32_16x16x32_bf16 v[58:61], v[30:33], v[62:65], v[38:41]
	s_setprio 0
	s_barrier
	s_add_i32 s61, s61, s33
	s_nop 3
	ds_read_b128 v[38:41], v149 offset:16384
	ds_read_b128 v[54:57], v149 offset:17408
	ds_read_b128 v[62:65], v149 offset:18432
	ds_read_b128 v[86:89], v149 offset:19456
	ds_read_b128 v[98:101], v149 offset:20480
	ds_read_b128 v[106:109], v149 offset:21504
	ds_read_b128 v[114:117], v149 offset:22528
	ds_read_b128 v[118:121], v149 offset:23552
	s_mov_b32 m0, s61
	v_lshl_add_u64 v[122:123], s[46:47], 0, v[132:133]
	global_load_lds_dwordx4 v[122:123], off
	v_lshl_add_u64 v[122:123], s[46:47], 0, v[130:131]
	s_add_i32 s46, s61, 0x2000
	s_add_u32 s50, s30, 0x40100
	s_mov_b32 m0, s46
	s_addc_u32 s51, s31, 0
	s_add_i32 s47, s52, s33
	global_load_lds_dwordx4 v[122:123], off
	s_mov_b32 m0, s47
	v_lshl_add_u64 v[122:123], s[50:51], 0, v[132:133]
	s_add_i32 s62, s47, 0x2000
	global_load_lds_dwordx4 v[122:123], off
	v_lshl_add_u64 v[122:123], s[50:51], 0, v[130:131]
	s_mov_b32 m0, s62
	s_nop 0
	global_load_lds_dwordx4 v[122:123], off
	s_mov_b32 m0, s23
	v_lshl_add_u64 v[122:123], s[18:19], 0, v[132:133]
	global_load_lds_dwordx4 v[122:123], off
	v_lshl_add_u64 v[122:123], s[18:19], 0, v[130:131]
	s_mov_b32 m0, s29
	s_nop 0
	global_load_lds_dwordx4 v[122:123], off
	s_waitcnt vmcnt(16)
	s_waitcnt lgkmcnt(0)
	s_barrier
	s_setprio 1
	s_waitcnt lgkmcnt(0)
	v_mfma_f32_16x16x32_bf16 v[122:125], v[2:5], v[38:41], 0
	v_mfma_f32_16x16x32_bf16 v[150:153], v[6:9], v[54:57], v[122:125]
	v_mfma_f32_16x16x32_bf16 v[122:125], v[10:13], v[38:41], 0
	v_mfma_f32_16x16x32_bf16 v[154:157], v[14:17], v[54:57], v[122:125]
	v_mfma_f32_16x16x32_bf16 v[122:125], v[2:5], v[62:65], 0
	v_mfma_f32_16x16x32_bf16 v[158:161], v[6:9], v[86:89], v[122:125]
	v_mfma_f32_16x16x32_bf16 v[122:125], v[10:13], v[62:65], 0
	v_mfma_f32_16x16x32_bf16 v[162:165], v[14:17], v[86:89], v[122:125]
	v_mfma_f32_16x16x32_bf16 v[122:125], v[2:5], v[98:101], 0
	v_mfma_f32_16x16x32_bf16 v[2:5], v[2:5], v[114:117], 0
	v_mfma_f32_16x16x32_bf16 v[166:169], v[6:9], v[106:109], v[122:125]
	v_mfma_f32_16x16x32_bf16 v[2:5], v[6:9], v[118:121], v[2:5]
	v_mfma_f32_16x16x32_bf16 v[6:9], v[10:13], v[114:117], 0
	v_mfma_f32_16x16x32_bf16 v[122:125], v[10:13], v[98:101], 0
	v_mfma_f32_16x16x32_bf16 v[6:9], v[14:17], v[118:121], v[6:9]
	v_mfma_f32_16x16x32_bf16 v[170:173], v[14:17], v[106:109], v[122:125]
	s_setprio 0
	s_setprio 1
	v_mfma_f32_16x16x32_bf16 v[10:13], v[18:21], v[38:41], 0
	v_mfma_f32_16x16x32_bf16 v[174:177], v[22:25], v[54:57], v[10:13]
	v_mfma_f32_16x16x32_bf16 v[10:13], v[26:29], v[38:41], 0
	v_mfma_f32_16x16x32_bf16 v[178:181], v[30:33], v[54:57], v[10:13]
	v_mfma_f32_16x16x32_bf16 v[10:13], v[18:21], v[62:65], 0
	v_mfma_f32_16x16x32_bf16 v[182:185], v[22:25], v[86:89], v[10:13]
	v_mfma_f32_16x16x32_bf16 v[10:13], v[26:29], v[62:65], 0
	v_mfma_f32_16x16x32_bf16 v[186:189], v[30:33], v[86:89], v[10:13]
	v_mfma_f32_16x16x32_bf16 v[10:13], v[18:21], v[98:101], 0
	v_mfma_f32_16x16x32_bf16 v[194:197], v[22:25], v[106:109], v[10:13]
	v_mfma_f32_16x16x32_bf16 v[10:13], v[26:29], v[98:101], 0
	v_mfma_f32_16x16x32_bf16 v[198:201], v[30:33], v[106:109], v[10:13]
	v_mfma_f32_16x16x32_bf16 v[10:13], v[18:21], v[114:117], 0
	v_mfma_f32_16x16x32_bf16 v[202:205], v[22:25], v[118:121], v[10:13]
	v_mfma_f32_16x16x32_bf16 v[10:13], v[26:29], v[114:117], 0
	v_mfma_f32_16x16x32_bf16 v[214:217], v[30:33], v[118:121], v[10:13]
	s_setprio 0
	s_barrier
	s_add_i32 s63, 0, 0x18000
	s_add_i32 s65, 0, 0x1c000
	v_add_u32_e32 v136, s63, v146
	v_add_u32_e32 v137, s65, v146
	s_nop 0
	ds_read_b128 v[10:13], v136
	ds_read_b128 v[14:17], v136 offset:1024
	ds_read_b128 v[18:21], v136 offset:2048
	ds_read_b128 v[22:25], v136 offset:3072
	ds_read_b128 v[218:221], v137
	ds_read_b128 v[222:225], v137 offset:1024
	ds_read_b128 v[226:229], v137 offset:2048
	ds_read_b128 v[230:233], v137 offset:3072
	s_add_u32 s18, s34, 0x40100
	s_addc_u32 s19, s35, 0
	s_mov_b32 m0, s55
	ds_read_b128 v[26:29], v149 offset:32768
	ds_read_b128 v[30:33], v149 offset:33792
	ds_read_b128 v[62:65], v149 offset:34816
	ds_read_b128 v[234:237], v149 offset:35840
	ds_read_b128 v[238:241], v149 offset:36864
	ds_read_b128 v[242:245], v149 offset:37888
	ds_read_b128 v[246:249], v149 offset:38912
	ds_read_b128 v[206:209], v149 offset:39936
	s_nop 0
	v_lshl_add_u64 v[38:39], s[18:19], 0, v[132:133]
	global_load_lds_dwordx4 v[38:39], off
	v_lshl_add_u64 v[38:39], s[18:19], 0, v[130:131]
	s_mov_b32 m0, s56
	s_nop 0
	global_load_lds_dwordx4 v[38:39], off
	s_waitcnt vmcnt(8)
	s_waitcnt lgkmcnt(0)
	s_barrier
	s_setprio 1
	s_waitcnt lgkmcnt(0)
	v_mfma_f32_16x16x32_bf16 v[38:41], v[10:13], v[26:29], v[66:69]
	v_mfma_f32_16x16x32_bf16 v[122:125], v[14:17], v[30:33], v[38:41]
	v_mfma_f32_16x16x32_bf16 v[38:41], v[18:21], v[26:29], v[70:73]
	v_mfma_f32_16x16x32_bf16 v[114:117], v[22:25], v[30:33], v[38:41]
	v_mfma_f32_16x16x32_bf16 v[38:41], v[10:13], v[62:65], v[74:77]
	v_mfma_f32_16x16x32_bf16 v[106:109], v[14:17], v[234:237], v[38:41]
	v_mfma_f32_16x16x32_bf16 v[38:41], v[18:21], v[62:65], v[78:81]
	v_mfma_f32_16x16x32_bf16 v[98:101], v[22:25], v[234:237], v[38:41]
	v_mfma_f32_16x16x32_bf16 v[38:41], v[10:13], v[238:241], v[82:85]
	v_mfma_f32_16x16x32_bf16 v[86:89], v[14:17], v[242:245], v[38:41]
	v_mfma_f32_16x16x32_bf16 v[38:41], v[18:21], v[238:241], v[90:93]
	v_mfma_f32_16x16x32_bf16 v[70:73], v[22:25], v[242:245], v[38:41]
	v_mfma_f32_16x16x32_bf16 v[38:41], v[10:13], v[246:249], v[94:97]
	v_mfma_f32_16x16x32_bf16 v[54:57], v[14:17], v[206:209], v[38:41]
	v_mfma_f32_16x16x32_bf16 v[38:41], v[18:21], v[246:249], v[102:105]
	v_mfma_f32_16x16x32_bf16 v[38:41], v[22:25], v[206:209], v[38:41]
	s_setprio 0
	s_setprio 1
	v_mfma_f32_16x16x32_bf16 v[66:69], v[218:221], v[26:29], v[110:113]
	v_mfma_f32_16x16x32_bf16 v[26:29], v[226:229], v[26:29], v[34:37]
	v_mfma_f32_16x16x32_bf16 v[118:121], v[230:233], v[30:33], v[26:29]
	v_mfma_f32_16x16x32_bf16 v[26:29], v[218:221], v[62:65], v[138:141]
	v_mfma_f32_16x16x32_bf16 v[110:113], v[222:225], v[234:237], v[26:29]
	v_mfma_f32_16x16x32_bf16 v[26:29], v[226:229], v[62:65], v[42:45]
	v_mfma_f32_16x16x32_bf16 v[102:105], v[230:233], v[234:237], v[26:29]
	v_mfma_f32_16x16x32_bf16 v[26:29], v[218:221], v[238:241], v[46:49]
	v_mfma_f32_16x16x32_bf16 v[90:93], v[222:225], v[242:245], v[26:29]
	v_mfma_f32_16x16x32_bf16 v[26:29], v[226:229], v[238:241], v[50:53]
	v_mfma_f32_16x16x32_bf16 v[74:77], v[230:233], v[242:245], v[26:29]
	v_mfma_f32_16x16x32_bf16 v[26:29], v[218:221], v[246:249], v[142:145]
	v_mfma_f32_16x16x32_bf16 v[62:65], v[222:225], v[206:209], v[26:29]
	v_mfma_f32_16x16x32_bf16 v[26:29], v[226:229], v[246:249], v[58:61]
	v_mfma_f32_16x16x32_bf16 v[126:129], v[222:225], v[30:33], v[66:69]
	v_mfma_f32_16x16x32_bf16 v[50:53], v[230:233], v[206:209], v[26:29]
	s_setprio 0
	s_barrier
;     ...
;         PG8_TRIP(0, true);
; #pragma unroll 1
;         for (int t = 2; t < nt; t += 2) PG8_TRIP(t, false);
	s_add_u32 s18, s30, 0x180
	s_addc_u32 s19, s31, 0
	s_add_i32 s63, s63, s33
	ds_read_b128 v[34:37], v149 offset:49152
	ds_read_b128 v[42:45], v149 offset:50176
	ds_read_b128 v[138:141], v149 offset:51200
	ds_read_b128 v[142:145], v149 offset:52224
	ds_read_b128 v[206:209], v149 offset:53248
	ds_read_b128 v[234:237], v149 offset:54272
	ds_read_b128 v[238:241], v149 offset:55296
	ds_read_b128 v[242:245], v149 offset:56320
	s_mov_b32 m0, s63
	v_lshl_add_u64 v[26:27], s[18:19], 0, v[132:133]
	s_add_i32 s64, s63, 0x2000
	global_load_lds_dwordx4 v[26:27], off
	v_lshl_add_u64 v[26:27], s[18:19], 0, v[130:131]
	s_add_u32 s18, s30, 0x40180
	s_mov_b32 m0, s64
	s_addc_u32 s19, s31, 0
	s_add_i32 s65, s65, s33
	global_load_lds_dwordx4 v[26:27], off
	s_mov_b32 m0, s65
	v_lshl_add_u64 v[26:27], s[18:19], 0, v[132:133]
	s_add_i32 s66, s65, 0x2000
	global_load_lds_dwordx4 v[26:27], off
	v_lshl_add_u64 v[26:27], s[18:19], 0, v[130:131]
	s_mov_b32 m0, s66
	s_nop 0
	global_load_lds_dwordx4 v[26:27], off
	s_mov_b32 m0, s57
	v_lshl_add_u64 v[26:27], s[42:43], 0, v[132:133]
	global_load_lds_dwordx4 v[26:27], off
	v_lshl_add_u64 v[26:27], s[42:43], 0, v[130:131]
	s_mov_b32 m0, s58
	s_nop 0
	global_load_lds_dwordx4 v[26:27], off
	s_waitcnt vmcnt(8)
	s_waitcnt lgkmcnt(0)
	s_barrier
	s_setprio 1
	s_waitcnt lgkmcnt(0)
	v_mfma_f32_16x16x32_bf16 v[26:29], v[10:13], v[34:37], v[150:153]
	v_mfma_f32_16x16x32_bf16 v[94:97], v[14:17], v[42:45], v[26:29]
	v_mfma_f32_16x16x32_bf16 v[26:29], v[18:21], v[34:37], v[154:157]
	v_mfma_f32_16x16x32_bf16 v[82:85], v[22:25], v[42:45], v[26:29]
	v_mfma_f32_16x16x32_bf16 v[26:29], v[10:13], v[138:141], v[158:161]
	v_mfma_f32_16x16x32_bf16 v[58:61], v[14:17], v[142:145], v[26:29]
	v_mfma_f32_16x16x32_bf16 v[26:29], v[18:21], v[138:141], v[162:165]
	v_mfma_f32_16x16x32_bf16 v[46:49], v[22:25], v[142:145], v[26:29]
	v_mfma_f32_16x16x32_bf16 v[26:29], v[10:13], v[206:209], v[166:169]
	v_mfma_f32_16x16x32_bf16 v[2:5], v[10:13], v[238:241], v[2:5]
	v_mfma_f32_16x16x32_bf16 v[30:33], v[14:17], v[234:237], v[26:29]
	v_mfma_f32_16x16x32_bf16 v[26:29], v[18:21], v[206:209], v[170:173]
	v_mfma_f32_16x16x32_bf16 v[14:17], v[14:17], v[242:245], v[2:5]
	v_mfma_f32_16x16x32_bf16 v[2:5], v[18:21], v[238:241], v[6:9]
	v_mfma_f32_16x16x32_bf16 v[26:29], v[22:25], v[234:237], v[26:29]
	v_mfma_f32_16x16x32_bf16 v[10:13], v[22:25], v[242:245], v[2:5]
	s_setprio 0
	s_setprio 1
	v_mfma_f32_16x16x32_bf16 v[2:5], v[218:221], v[34:37], v[174:177]
	v_mfma_f32_16x16x32_bf16 v[78:81], v[222:225], v[42:45], v[2:5]
	v_mfma_f32_16x16x32_bf16 v[2:5], v[226:229], v[34:37], v[178:181]
	v_mfma_f32_16x16x32_bf16 v[66:69], v[230:233], v[42:45], v[2:5]
	v_mfma_f32_16x16x32_bf16 v[2:5], v[218:221], v[138:141], v[182:185]
	v_mfma_f32_16x16x32_bf16 v[42:45], v[222:225], v[142:145], v[2:5]
	v_mfma_f32_16x16x32_bf16 v[2:5], v[226:229], v[138:141], v[186:189]
	v_mfma_f32_16x16x32_bf16 v[34:37], v[230:233], v[142:145], v[2:5]
	v_mfma_f32_16x16x32_bf16 v[2:5], v[218:221], v[206:209], v[194:197]
	v_mfma_f32_16x16x32_bf16 v[22:25], v[222:225], v[234:237], v[2:5]
	v_mfma_f32_16x16x32_bf16 v[2:5], v[226:229], v[206:209], v[198:201]
	v_mfma_f32_16x16x32_bf16 v[18:21], v[230:233], v[234:237], v[2:5]
	v_mfma_f32_16x16x32_bf16 v[2:5], v[218:221], v[238:241], v[202:205]
	v_mfma_f32_16x16x32_bf16 v[6:9], v[222:225], v[242:245], v[2:5]
	v_mfma_f32_16x16x32_bf16 v[2:5], v[226:229], v[238:241], v[214:217]
	v_mfma_f32_16x16x32_bf16 v[2:5], v[230:233], v[242:245], v[2:5]
	s_setprio 0
	s_barrier
	s_mov_b32 s67, 0

; #define LDS_WAIT() asm volatile("s_waitcnt lgkmcnt(0)" ::: "memory")
; #define PG8_STAGE(bufoff, gbase, voff) do { const char* gb_ = (const char*)(gbase); asm volatile("" : "+s"(gb_));     \
;         _Pragma("unroll") for (int _i = 0; _i < 2; ++_i) \
;         __builtin_amdgcn_global_load_lds((const unsigned*)(gb_ + (voff)[_i]), (LAS unsigned*)(lds + (bufoff) + ldsw + _i * 8192), 16, 0, 0); } while (0)
; #define PG8_STAGE_A(bufoff, gbase, h, vo) do { if constexpr (GATHER) { PG8_STAGE(bufoff, gbase, (vo)[h]); } else { PG8_STAGE(bufoff, (gbase) + (h) * hstep, voffA); } } while (0)
; #define PG8_WAIT_V(n) asm volatile("s_waitcnt vmcnt(" #n ")" ::: "memory")
; #define PG8_BAR __builtin_amdgcn_s_barrier()
;     ...
;     const char* cA = GATHER ? (const char*)A : (const char*)A + (size_t)cur.pm * tstep; const char* cB = (const char*)Bt + (size_t)cur.pn * tstep;
;     if constexpr (GATHER) { LDS_WAIT(); }
;     if constexpr (SP2) {
;         PG8_STAGE(PG8_SB(0, 0), cB + PG8_KO(0), voffB); PG8_STAGE(PG8_SB(0, 1), cB + hstep + PG8_KO(0), voffB); PG8_STAGE_A(PG8_SA(0, 0), cA + PG8_KO(0), 0, cvo); PG8_STAGE_A(PG8_SA(0, 1), cA + PG8_KO(0), 1, cvo);
;         if (wr == 1) PG8_BAR;
;         PG8_WAIT_V(2); PG8_BAR;
;         PG8_STAGE(PG8_SB(1, 0), cB + PG8_KO(1), voffB); PG8_STAGE_A(PG8_SA(1, 0), cA + PG8_KO(1), 0, cvo); PG8_STAGE(PG8_SB(1, 1), cB + hstep + PG8_KO(1), voffB);
;         PG8_WAIT_V(6); PG8_BAR;
.LBB0_664:
	s_lshl_b32 s12, s44, 8
	s_lshl_b64 s[18:19], s[12:13], 2
	v_readlane_b32 s3, v253, 51
	s_add_u32 s18, s3, s18
	v_readlane_b32 s3, v253, 52
	s_addc_u32 s19, s3, s19
	s_and_b32 s63, s10, 3
	s_lshl_b32 s64, s33, 6
	s_lshl_b32 s3, s33, 13
	s_lshl_b32 s7, s63, 12
	s_add_u32 s10, s8, 0x80
	v_mov_b32_e32 v163, v191
	s_addc_u32 s11, s9, 0
	s_waitcnt vmcnt(2)
	s_barrier
	s_add_i32 m0, s46, 0x18000
	v_lshl_add_u64 v[4:5], s[10:11], 0, v[162:163]
	v_mov_b32_e32 v165, v191
	global_load_lds_dwordx4 v[4:5], off
	s_add_i32 m0, s46, 0x1a000
	v_lshl_add_u64 v[4:5], s[10:11], 0, v[164:165]
	s_add_u32 s10, s28, 0x80
	s_addc_u32 s11, s29, 0
	s_add_i32 s65, s46, 0x8000
	global_load_lds_dwordx4 v[4:5], off
	s_mov_b32 m0, s65
	v_lshl_add_u64 v[4:5], s[10:11], 0, v[162:163]
	s_add_i32 s66, s46, 0xa000
	global_load_lds_dwordx4 v[4:5], off
	v_lshl_add_u64 v[4:5], s[10:11], 0, v[164:165]
	s_add_u32 s10, s8, 0x20080
	s_mov_b32 m0, s66
	s_addc_u32 s11, s9, 0
	global_load_lds_dwordx4 v[4:5], off
	s_add_i32 m0, s46, 0x1c000
	v_lshl_add_u64 v[4:5], s[10:11], 0, v[162:163]
	global_load_lds_dwordx4 v[4:5], off
	v_lshl_add_u64 v[4:5], s[10:11], 0, v[164:165]
	s_add_i32 m0, s46, 0x1e000
	v_bfe_u32 v3, v2, 4, 2
	global_load_lds_dwordx4 v[4:5], off
	v_and_b32_e32 v1, 15, v2
	v_lshlrev_b32_e32 v190, 4, v3
	v_lshlrev_b32_e32 v2, 2, v2
	s_cmpk_lt_u32 s1, 0x100
	v_lshl_or_b32 v4, v1, 6, v190
	v_and_b32_e32 v2, 32, v2
	s_cselect_b64 s[10:11], -1, 0
	s_cmp_gt_u32 s63, 1
	v_bitop3_b32 v5, v4, s3, v2 bitop3:0xde
	s_waitcnt vmcnt(0)
	s_cselect_b64 s[22:23], -1, 0
	s_add_i32 s3, 0, 0x20400
	v_add_u32_e32 v170, s3, v190
	v_bitop3_b32 v167, v4, s7, v2 bitop3:0xde
	v_lshlrev_b32_e32 v166, 2, v3
	s_mov_b32 s1, s13
	v_lshl_add_u64 v[168:169], s[18:19], 0, v[190:191]
	s_lshr_b32 s67, s0, 3
	v_lshl_add_u32 v171, v1, 7, v170
	s_mov_b32 s68, 0
	v_add_u32_e32 v172, 0, v5
	s_xor_b64 s[22:23], s[22:23], -1
	s_barrier
	s_branch .LBB0_667

.LBB0_669:
	s_ashr_i32 s53, s52, 31
	s_lshl_b64 s[18:19], s[52:53], 18
	s_add_u32 s54, s96, s18
	s_addc_u32 s55, s97, s19
	s_ashr_i32 s35, s34, 31
	s_lshl_b64 s[18:19], s[34:35], 18
	s_add_u32 s56, s17, s18
	s_addc_u32 s57, s25, s19
	s_add_u32 s18, s28, 0x100
	s_addc_u32 s19, s29, 0
	s_add_u32 s38, s28, 0x180
	s_addc_u32 s39, s29, 0
	s_add_u32 s40, s8, 0x100
	s_addc_u32 s41, s9, 0
	s_add_i32 s12, 0, 0x10000
	s_add_i32 s53, 0, 0x14000
	v_add_u32_e32 v173, s12, v167
	v_add_u32_e32 v174, s53, v167
	ds_read_b128 v[2:5], v173
	ds_read_b128 v[6:9], v173 offset:1024
	ds_read_b128 v[10:13], v173 offset:2048
	ds_read_b128 v[14:17], v173 offset:3072
	ds_read_b128 v[18:21], v174
	ds_read_b128 v[22:25], v174 offset:1024
	ds_read_b128 v[26:29], v174 offset:2048
	ds_read_b128 v[30:33], v174 offset:3072
	s_mov_b64 s[30:31], 0x100
	s_add_u32 s42, s28, 0x20080
	s_addc_u32 s43, s29, 0
	s_add_i32 s3, s46, 0xc000
	ds_read_b128 v[34:37], v172
	ds_read_b128 v[38:41], v172 offset:1024
	ds_read_b128 v[42:45], v172 offset:2048
	ds_read_b128 v[46:49], v172 offset:3072
	ds_read_b128 v[50:53], v172 offset:4096
	ds_read_b128 v[54:57], v172 offset:5120
	ds_read_b128 v[58:61], v172 offset:6144
	ds_read_b128 v[62:65], v172 offset:7168
	s_mov_b32 m0, s3
	v_lshl_add_u64 v[66:67], s[42:43], 0, v[162:163]
	s_add_i32 s7, s46, 0xe000
	global_load_lds_dwordx4 v[66:67], off
	v_lshl_add_u64 v[66:67], s[42:43], 0, v[164:165]
	s_mov_b32 m0, s7
	s_nop 0
	global_load_lds_dwordx4 v[66:67], off
	s_waitcnt vmcnt(40)
	s_waitcnt lgkmcnt(0)
	s_barrier
	s_setprio 1
	s_waitcnt lgkmcnt(0)
	v_mfma_f32_16x16x128_f8f6f4 v[146:149], v[2:9], v[34:41], 0
	v_mfma_f32_16x16x128_f8f6f4 v[150:153], v[10:17], v[34:41], 0
	v_mfma_f32_16x16x128_f8f6f4 v[134:137], v[2:9], v[42:49], 0
	v_mfma_f32_16x16x128_f8f6f4 v[130:133], v[10:17], v[42:49], 0
	v_mfma_f32_16x16x128_f8f6f4 v[118:121], v[2:9], v[50:57], 0
	v_mfma_f32_16x16x128_f8f6f4 v[114:117], v[10:17], v[50:57], 0
	v_mfma_f32_16x16x128_f8f6f4 v[102:105], v[2:9], v[58:65], 0
	v_mfma_f32_16x16x128_f8f6f4 v[98:101], v[10:17], v[58:65], 0
	s_setprio 0
	s_setprio 1
	v_mfma_f32_16x16x128_f8f6f4 v[154:157], v[18:25], v[34:41], 0
	v_mfma_f32_16x16x128_f8f6f4 v[158:161], v[26:33], v[34:41], 0
	v_mfma_f32_16x16x128_f8f6f4 v[142:145], v[18:25], v[42:49], 0
	v_mfma_f32_16x16x128_f8f6f4 v[138:141], v[26:33], v[42:49], 0
	v_mfma_f32_16x16x128_f8f6f4 v[126:129], v[18:25], v[50:57], 0
	v_mfma_f32_16x16x128_f8f6f4 v[122:125], v[26:33], v[50:57], 0
	v_mfma_f32_16x16x128_f8f6f4 v[110:113], v[18:25], v[58:65], 0
	v_mfma_f32_16x16x128_f8f6f4 v[106:109], v[26:33], v[58:65], 0
	s_setprio 0
	s_barrier
	s_add_i32 s12, s12, s45
	ds_read_b128 v[74:77], v172 offset:16384
	ds_read_b128 v[78:81], v172 offset:17408
	ds_read_b128 v[176:179], v172 offset:18432
	ds_read_b128 v[180:183], v172 offset:19456
	ds_read_b128 v[194:197], v172 offset:20480
	ds_read_b128 v[198:201], v172 offset:21504
	ds_read_b128 v[214:217], v172 offset:22528
	ds_read_b128 v[218:221], v172 offset:23552
	s_mov_b32 m0, s12
	v_lshl_add_u64 v[34:35], s[40:41], 0, v[162:163]
	s_add_i32 s35, s12, 0x2000
	global_load_lds_dwordx4 v[34:35], off
	v_lshl_add_u64 v[34:35], s[40:41], 0, v[164:165]
	s_add_u32 s40, s8, 0x20100
	s_mov_b32 m0, s35
	s_addc_u32 s41, s9, 0
	s_add_i32 s53, s53, s45
	global_load_lds_dwordx4 v[34:35], off
	s_mov_b32 m0, s53
	v_lshl_add_u64 v[34:35], s[40:41], 0, v[162:163]
	s_add_i32 s69, s53, 0x2000
	global_load_lds_dwordx4 v[34:35], off
	v_lshl_add_u64 v[34:35], s[40:41], 0, v[164:165]
	s_mov_b32 m0, s69
	s_nop 0
	global_load_lds_dwordx4 v[34:35], off
	s_mov_b32 m0, s46
	v_lshl_add_u64 v[34:35], s[18:19], 0, v[162:163]
	global_load_lds_dwordx4 v[34:35], off
	v_lshl_add_u64 v[34:35], s[18:19], 0, v[164:165]
	s_mov_b32 m0, s47
	s_nop 0
	global_load_lds_dwordx4 v[34:35], off
	s_waitcnt vmcnt(40)
	s_waitcnt lgkmcnt(0)
	s_barrier
	s_setprio 1
	s_waitcnt lgkmcnt(0)
	v_mfma_f32_16x16x128_f8f6f4 v[86:89], v[2:9], v[74:81], 0
	v_mfma_f32_16x16x128_f8f6f4 v[82:85], v[10:17], v[74:81], 0
	v_mfma_f32_16x16x128_f8f6f4 v[70:73], v[2:9], v[176:183], 0
	v_mfma_f32_16x16x128_f8f6f4 v[66:69], v[10:17], v[176:183], 0
	v_mfma_f32_16x16x128_f8f6f4 v[58:61], v[2:9], v[194:201], 0
	v_mfma_f32_16x16x128_f8f6f4 v[50:53], v[10:17], v[194:201], 0
	v_mfma_f32_16x16x128_f8f6f4 v[46:49], v[2:9], v[214:221], 0
	v_mfma_f32_16x16x128_f8f6f4 v[38:41], v[10:17], v[214:221], 0
	s_setprio 0
	s_setprio 1
	v_mfma_f32_16x16x128_f8f6f4 v[94:97], v[18:25], v[74:81], 0
	v_mfma_f32_16x16x128_f8f6f4 v[90:93], v[26:33], v[74:81], 0
	v_mfma_f32_16x16x128_f8f6f4 v[78:81], v[18:25], v[176:183], 0
	v_mfma_f32_16x16x128_f8f6f4 v[74:77], v[26:33], v[176:183], 0
	v_mfma_f32_16x16x128_f8f6f4 v[62:65], v[18:25], v[194:201], 0
	v_mfma_f32_16x16x128_f8f6f4 v[54:57], v[26:33], v[194:201], 0
	v_mfma_f32_16x16x128_f8f6f4 v[42:45], v[18:25], v[214:221], 0
	v_mfma_f32_16x16x128_f8f6f4 v[34:37], v[26:33], v[214:221], 0
	s_setprio 0
	s_barrier
	s_add_i32 s42, 0, 0x18000
	s_add_i32 s70, 0, 0x1c000
	v_add_u32_e32 v175, s42, v167
	v_add_u32_e32 v176, s70, v167
	ds_read_b128 v[26:29], v175
	ds_read_b128 v[30:33], v175 offset:1024
	ds_read_b128 v[18:21], v175 offset:2048
	ds_read_b128 v[22:25], v175 offset:3072
	ds_read_b128 v[10:13], v176
	ds_read_b128 v[14:17], v176 offset:1024
	ds_read_b128 v[2:5], v176 offset:2048
	ds_read_b128 v[6:9], v176 offset:3072
	s_add_u32 s18, s28, 0x20100
	s_addc_u32 s19, s29, 0
	s_mov_b32 m0, s61
	ds_read_b128 v[178:181], v172 offset:32768
	ds_read_b128 v[182:185], v172 offset:33792
	ds_read_b128 v[194:197], v172 offset:34816
	ds_read_b128 v[198:201], v172 offset:35840
	ds_read_b128 v[214:217], v172 offset:36864
	ds_read_b128 v[218:221], v172 offset:37888
	ds_read_b128 v[222:225], v172 offset:38912
	ds_read_b128 v[226:229], v172 offset:39936
	s_nop 0
	v_lshl_add_u64 v[186:187], s[18:19], 0, v[162:163]
	global_load_lds_dwordx4 v[186:187], off
	v_lshl_add_u64 v[186:187], s[18:19], 0, v[164:165]
	s_mov_b32 m0, s62
	s_nop 0
	global_load_lds_dwordx4 v[186:187], off
	s_waitcnt vmcnt(8)
	s_waitcnt lgkmcnt(0)
	s_barrier
	s_setprio 1
	s_waitcnt lgkmcnt(0)
	v_mfma_f32_16x16x128_f8f6f4 v[146:149], v[26:33], v[178:185], v[146:149]
	v_mfma_f32_16x16x128_f8f6f4 v[150:153], v[18:25], v[178:185], v[150:153]
	v_mfma_f32_16x16x128_f8f6f4 v[134:137], v[26:33], v[194:201], v[134:137]
	v_mfma_f32_16x16x128_f8f6f4 v[130:133], v[18:25], v[194:201], v[130:133]
	v_mfma_f32_16x16x128_f8f6f4 v[118:121], v[26:33], v[214:221], v[118:121]
	v_mfma_f32_16x16x128_f8f6f4 v[114:117], v[18:25], v[214:221], v[114:117]
	v_mfma_f32_16x16x128_f8f6f4 v[102:105], v[26:33], v[222:229], v[102:105]
	v_mfma_f32_16x16x128_f8f6f4 v[98:101], v[18:25], v[222:229], v[98:101]
	s_setprio 0
	s_setprio 1
	v_mfma_f32_16x16x128_f8f6f4 v[154:157], v[10:17], v[178:185], v[154:157]
	v_mfma_f32_16x16x128_f8f6f4 v[158:161], v[2:9], v[178:185], v[158:161]
	v_mfma_f32_16x16x128_f8f6f4 v[142:145], v[10:17], v[194:201], v[142:145]
	v_mfma_f32_16x16x128_f8f6f4 v[138:141], v[2:9], v[194:201], v[138:141]
	v_mfma_f32_16x16x128_f8f6f4 v[126:129], v[10:17], v[214:221], v[126:129]
	v_mfma_f32_16x16x128_f8f6f4 v[122:125], v[2:9], v[214:221], v[122:125]
	v_mfma_f32_16x16x128_f8f6f4 v[110:113], v[10:17], v[222:229], v[110:113]
	v_mfma_f32_16x16x128_f8f6f4 v[106:109], v[2:9], v[222:229], v[106:109]
	s_setprio 0
	s_barrier
	s_add_u32 s40, s8, 0x180
	s_addc_u32 s41, s9, 0
	s_add_i32 s18, s42, s45
	ds_read_b128 v[178:181], v172 offset:49152
	ds_read_b128 v[182:185], v172 offset:50176
	ds_read_b128 v[194:197], v172 offset:51200
	ds_read_b128 v[198:201], v172 offset:52224
	ds_read_b128 v[214:217], v172 offset:53248
	ds_read_b128 v[218:221], v172 offset:54272
	ds_read_b128 v[222:225], v172 offset:55296
	ds_read_b128 v[226:229], v172 offset:56320
	s_mov_b32 m0, s18
	v_lshl_add_u64 v[186:187], s[40:41], 0, v[162:163]
	s_add_i32 s19, s18, 0x2000
	global_load_lds_dwordx4 v[186:187], off
	v_lshl_add_u64 v[186:187], s[40:41], 0, v[164:165]
	s_add_u32 s40, s8, 0x20180
	s_mov_b32 m0, s19
	s_addc_u32 s41, s9, 0
	s_add_i32 s70, s70, s45
	global_load_lds_dwordx4 v[186:187], off
	s_mov_b32 m0, s70
	v_lshl_add_u64 v[186:187], s[40:41], 0, v[162:163]
	s_add_i32 s71, s70, 0x2000
	global_load_lds_dwordx4 v[186:187], off
	v_lshl_add_u64 v[186:187], s[40:41], 0, v[164:165]
	s_mov_b32 m0, s71
	s_nop 0
	global_load_lds_dwordx4 v[186:187], off
	s_mov_b32 m0, s65
	v_lshl_add_u64 v[186:187], s[38:39], 0, v[162:163]
	global_load_lds_dwordx4 v[186:187], off
	v_lshl_add_u64 v[186:187], s[38:39], 0, v[164:165]
	s_mov_b32 m0, s66
	s_nop 0
	global_load_lds_dwordx4 v[186:187], off
	s_waitcnt vmcnt(8)
	s_waitcnt lgkmcnt(0)
	s_barrier
	s_setprio 1
	s_waitcnt lgkmcnt(0)
	v_mfma_f32_16x16x128_f8f6f4 v[86:89], v[26:33], v[178:185], v[86:89]
	v_mfma_f32_16x16x128_f8f6f4 v[82:85], v[18:25], v[178:185], v[82:85]
	v_mfma_f32_16x16x128_f8f6f4 v[70:73], v[26:33], v[194:201], v[70:73]
	v_mfma_f32_16x16x128_f8f6f4 v[66:69], v[18:25], v[194:201], v[66:69]
	v_mfma_f32_16x16x128_f8f6f4 v[58:61], v[26:33], v[214:221], v[58:61]
	v_mfma_f32_16x16x128_f8f6f4 v[50:53], v[18:25], v[214:221], v[50:53]
	v_mfma_f32_16x16x128_f8f6f4 v[46:49], v[26:33], v[222:229], v[46:49]
	v_mfma_f32_16x16x128_f8f6f4 v[38:41], v[18:25], v[222:229], v[38:41]
	s_setprio 0
	s_setprio 1
	v_mfma_f32_16x16x128_f8f6f4 v[94:97], v[10:17], v[178:185], v[94:97]
	v_mfma_f32_16x16x128_f8f6f4 v[90:93], v[2:9], v[178:185], v[90:93]
	v_mfma_f32_16x16x128_f8f6f4 v[78:81], v[10:17], v[194:201], v[78:81]
	v_mfma_f32_16x16x128_f8f6f4 v[74:77], v[2:9], v[194:201], v[74:77]
	v_mfma_f32_16x16x128_f8f6f4 v[62:65], v[10:17], v[214:221], v[62:65]
	v_mfma_f32_16x16x128_f8f6f4 v[54:57], v[2:9], v[214:221], v[54:57]
	v_mfma_f32_16x16x128_f8f6f4 v[42:45], v[10:17], v[222:229], v[42:45]
	v_mfma_f32_16x16x128_f8f6f4 v[34:37], v[2:9], v[222:229], v[34:37]
	s_setprio 0
	s_barrier
	s_mov_b32 s72, 0

; #define PG8_STAGE(bufoff, gbase, voff) do { const char* gb_ = (const char*)(gbase); asm volatile("" : "+s"(gb_));     \
;         _Pragma("unroll") for (int _i = 0; _i < 2; ++_i) \
;         __builtin_amdgcn_global_load_lds((const unsigned*)(gb_ + (voff)[_i]), (LAS unsigned*)(lds + (bufoff) + ldsw + _i * 8192), 16, 0, 0); } while (0)
; #define PG8_STAGE_A(bufoff, gbase, h, vo) do { if constexpr (GATHER) { PG8_STAGE(bufoff, gbase, (vo)[h]); } else { PG8_STAGE(bufoff, (gbase) + (h) * hstep, voffA); } } while (0)
; #define PG8_WAIT_V(n) asm volatile("s_waitcnt vmcnt(" #n ")" ::: "memory")
; #define PG8_BAR __builtin_amdgcn_s_barrier()
;     ...
;     const int aoff = lds_byte(wr * 64 + fr, fq * 8), boff = lds_byte(wc * 32 + fr, fq * 8);
;     ...
;     if constexpr (SP2) {
;         PG8_STAGE(PG8_SB(0, 0), cB + PG8_KO(0), voffB); PG8_STAGE(PG8_SB(0, 1), cB + hstep + PG8_KO(0), voffB); PG8_STAGE_A(PG8_SA(0, 0), cA + PG8_KO(0), 0, cvo); PG8_STAGE_A(PG8_SA(0, 1), cA + PG8_KO(0), 1, cvo);
;         if (wr == 1) PG8_BAR;
;         PG8_WAIT_V(2); PG8_BAR;
;         PG8_STAGE(PG8_SB(1, 0), cB + PG8_KO(1), voffB); PG8_STAGE_A(PG8_SA(1, 0), cA + PG8_KO(1), 0, cvo); PG8_STAGE(PG8_SB(1, 1), cB + hstep + PG8_KO(1), voffB);
;         PG8_WAIT_V(6); PG8_BAR;
.LBB0_1058:
	v_lshrrev_b32_e32 v4, 1, v2
	v_and_b32_e32 v4, 24, v4
	s_lshl_b32 s3, s3, 5
	v_and_b32_e32 v3, 15, v2
	v_lshlrev_b32_e32 v5, 1, v4
	v_lshlrev_b32_e32 v2, 2, v2
	s_and_b32 s6, s3, 0x60
	v_lshl_or_b32 v1, s4, 6, v3
	v_lshl_or_b32 v3, v3, 6, v5
	s_lshl_b32 s4, s4, 13
	v_and_b32_e32 v2, 32, v2
	s_lshl_b32 s3, s6, 7
	v_bitop3_b32 v5, v3, s4, v2 bitop3:0xde
	s_add_u32 s4, s30, 0x80
	s_addc_u32 s5, s31, 0
	v_bitop3_b32 v193, v3, s3, v2 bitop3:0xde
	s_waitcnt vmcnt(2)
	s_barrier
	s_add_i32 m0, s23, 0x18000
	v_lshl_add_u64 v[2:3], s[4:5], 0, v[190:191]
	v_mov_b32_e32 v183, v191
	global_load_lds_dwordx4 v[2:3], off
	s_add_i32 m0, s23, 0x1a000
	v_lshl_add_u64 v[2:3], s[4:5], 0, v[182:183]
	s_add_u32 s4, s34, 0x80
	s_addc_u32 s5, s35, 0
	s_add_i32 s53, s23, 0x8000
	global_load_lds_dwordx4 v[2:3], off
	s_mov_b32 m0, s53
	v_lshl_add_u64 v[2:3], s[4:5], 0, v[190:191]
	s_add_i32 s54, s23, 0xa000
	global_load_lds_dwordx4 v[2:3], off
	v_lshl_add_u64 v[2:3], s[4:5], 0, v[182:183]
	s_add_u32 s4, s30, 0x40080
	s_mov_b32 m0, s54
	s_addc_u32 s5, s31, 0
	global_load_lds_dwordx4 v[2:3], off
	s_add_i32 m0, s23, 0x1c000
	v_lshl_add_u64 v[2:3], s[4:5], 0, v[190:191]
	global_load_lds_dwordx4 v[2:3], off
	v_lshl_add_u64 v[2:3], s[4:5], 0, v[182:183]
	s_add_i32 m0, s23, 0x1e000
	s_cmpk_lt_u32 s2, 0x100
	global_load_lds_dwordx4 v[2:3], off
	s_waitcnt vmcnt(0)
	s_cselect_b64 s[2:3], -1, 0
	v_or_b32_e32 v198, s6, v4
	s_mov_b32 s55, 0
	v_add_u32_e32 v199, 0, v5
	s_barrier
	s_branch .LBB0_1061

.LBB0_1063:
	s_ashr_i32 s7, s6, 31
	s_lshl_b64 s[8:9], s[6:7], 19
	s_add_u32 s8, s96, s8
	s_addc_u32 s9, s97, s9
	s_ashr_i32 s5, s4, 31
	s_lshl_b64 s[10:11], s[4:5], 19
	s_add_u32 s10, s25, s10
	s_addc_u32 s11, s33, s11
	s_add_u32 s18, s34, 0x100
	s_addc_u32 s19, s35, 0
	s_add_u32 s40, s34, 0x180
	s_addc_u32 s41, s35, 0
	s_add_u32 s42, s30, 0x100
	s_addc_u32 s43, s31, 0
	s_add_i32 s56, 0, 0x10000
	s_add_i32 s58, 0, 0x14000
	v_add_u32_e32 v98, s56, v193
	v_add_u32_e32 v99, s58, v193
	ds_read_b128 v[2:5], v98
	ds_read_b128 v[6:9], v98 offset:1024
	ds_read_b128 v[10:13], v98 offset:2048
	ds_read_b128 v[14:17], v98 offset:3072
	ds_read_b128 v[18:21], v99
	ds_read_b128 v[22:25], v99 offset:1024
	ds_read_b128 v[26:29], v99 offset:2048
	ds_read_b128 v[30:33], v99 offset:3072
	s_mov_b64 s[38:39], 0x100
	s_add_u32 s44, s34, 0x40080
	s_addc_u32 s45, s35, 0
	s_add_i32 s5, s23, 0xc000
	ds_read_b128 v[34:37], v199
	ds_read_b128 v[38:41], v199 offset:1024
	ds_read_b128 v[42:45], v199 offset:2048
	ds_read_b128 v[46:49], v199 offset:3072
	ds_read_b128 v[50:53], v199 offset:4096
	ds_read_b128 v[54:57], v199 offset:5120
	ds_read_b128 v[58:61], v199 offset:6144
	ds_read_b128 v[62:65], v199 offset:7168
	s_mov_b32 m0, s5
	v_lshl_add_u64 v[66:67], s[44:45], 0, v[190:191]
	s_add_i32 s7, s23, 0xe000
	global_load_lds_dwordx4 v[66:67], off
	v_lshl_add_u64 v[66:67], s[44:45], 0, v[182:183]
	s_mov_b32 m0, s7
	s_nop 0
	global_load_lds_dwordx4 v[66:67], off
	s_waitcnt vmcnt(24)
	s_waitcnt lgkmcnt(0)
	s_barrier
	s_setprio 1
	s_waitcnt lgkmcnt(0)
	v_mfma_f32_16x16x32_bf16 v[66:69], v[2:5], v[34:37], 0
	v_mfma_f32_16x16x32_bf16 v[70:73], v[10:13], v[34:37], 0
	v_mfma_f32_16x16x32_bf16 v[74:77], v[2:5], v[42:45], 0
	v_mfma_f32_16x16x32_bf16 v[78:81], v[10:13], v[42:45], 0
	v_mfma_f32_16x16x32_bf16 v[82:85], v[2:5], v[50:53], 0
	v_mfma_f32_16x16x32_bf16 v[86:89], v[10:13], v[50:53], 0
	v_mfma_f32_16x16x32_bf16 v[90:93], v[2:5], v[58:61], 0
	v_mfma_f32_16x16x32_bf16 v[66:69], v[6:9], v[38:41], v[66:69]
	v_mfma_f32_16x16x32_bf16 v[70:73], v[14:17], v[38:41], v[70:73]
	v_mfma_f32_16x16x32_bf16 v[74:77], v[6:9], v[46:49], v[74:77]
	v_mfma_f32_16x16x32_bf16 v[78:81], v[14:17], v[46:49], v[78:81]
	v_mfma_f32_16x16x32_bf16 v[82:85], v[6:9], v[54:57], v[82:85]
	v_mfma_f32_16x16x32_bf16 v[86:89], v[14:17], v[54:57], v[86:89]
	v_mfma_f32_16x16x32_bf16 v[102:105], v[6:9], v[62:65], v[90:93]
	v_mfma_f32_16x16x32_bf16 v[90:93], v[10:13], v[58:61], 0
	v_mfma_f32_16x16x32_bf16 v[106:109], v[14:17], v[62:65], v[90:93]
	s_setprio 0
	s_setprio 1
	v_mfma_f32_16x16x32_bf16 v[90:93], v[18:21], v[34:37], 0
	v_mfma_f32_16x16x32_bf16 v[34:37], v[26:29], v[34:37], 0
	v_mfma_f32_16x16x32_bf16 v[110:113], v[22:25], v[38:41], v[90:93]
	v_mfma_f32_16x16x32_bf16 v[34:37], v[30:33], v[38:41], v[34:37]
	v_mfma_f32_16x16x32_bf16 v[38:41], v[18:21], v[42:45], 0
	v_mfma_f32_16x16x32_bf16 v[42:45], v[26:29], v[42:45], 0
	v_mfma_f32_16x16x32_bf16 v[38:41], v[22:25], v[46:49], v[38:41]
	v_mfma_f32_16x16x32_bf16 v[42:45], v[30:33], v[46:49], v[42:45]
	v_mfma_f32_16x16x32_bf16 v[46:49], v[18:21], v[50:53], 0
	v_mfma_f32_16x16x32_bf16 v[50:53], v[26:29], v[50:53], 0
	v_mfma_f32_16x16x32_bf16 v[46:49], v[22:25], v[54:57], v[46:49]
	v_mfma_f32_16x16x32_bf16 v[50:53], v[30:33], v[54:57], v[50:53]
	v_mfma_f32_16x16x32_bf16 v[54:57], v[18:21], v[58:61], 0
	v_mfma_f32_16x16x32_bf16 v[58:61], v[26:29], v[58:61], 0
	v_mfma_f32_16x16x32_bf16 v[54:57], v[22:25], v[62:65], v[54:57]
	v_mfma_f32_16x16x32_bf16 v[58:61], v[30:33], v[62:65], v[58:61]
	s_setprio 0
	s_barrier
	s_add_i32 s56, s56, s48
	ds_read_b128 v[62:65], v199 offset:16384
	ds_read_b128 v[90:93], v199 offset:17408
	ds_read_b128 v[94:97], v199 offset:18432
	ds_read_b128 v[114:117], v199 offset:19456
	ds_read_b128 v[118:121], v199 offset:20480
	ds_read_b128 v[122:125], v199 offset:21504
	ds_read_b128 v[126:129], v199 offset:22528
	ds_read_b128 v[130:133], v199 offset:23552
	s_mov_b32 m0, s56
	v_lshl_add_u64 v[100:101], s[42:43], 0, v[190:191]
	s_add_i32 s57, s56, 0x2000
	global_load_lds_dwordx4 v[100:101], off
	v_lshl_add_u64 v[100:101], s[42:43], 0, v[182:183]
	s_add_u32 s42, s30, 0x40100
	s_mov_b32 m0, s57
	s_addc_u32 s43, s31, 0
	s_add_i32 s58, s58, s48
	global_load_lds_dwordx4 v[100:101], off
	s_mov_b32 m0, s58
	v_lshl_add_u64 v[100:101], s[42:43], 0, v[190:191]
	s_add_i32 s59, s58, 0x2000
	global_load_lds_dwordx4 v[100:101], off
	v_lshl_add_u64 v[100:101], s[42:43], 0, v[182:183]
	s_mov_b32 m0, s59
	s_nop 0
	global_load_lds_dwordx4 v[100:101], off
	s_mov_b32 m0, s23
	v_lshl_add_u64 v[100:101], s[18:19], 0, v[190:191]
	global_load_lds_dwordx4 v[100:101], off
	v_lshl_add_u64 v[100:101], s[18:19], 0, v[182:183]
	s_mov_b32 m0, s29
	s_nop 0
	global_load_lds_dwordx4 v[100:101], off
	s_waitcnt vmcnt(24)
	s_waitcnt lgkmcnt(0)
	s_barrier
	s_setprio 1
	s_waitcnt lgkmcnt(0)
	v_mfma_f32_16x16x32_bf16 v[134:137], v[2:5], v[62:65], 0
	v_mfma_f32_16x16x32_bf16 v[146:149], v[6:9], v[90:93], v[134:137]
	v_mfma_f32_16x16x32_bf16 v[134:137], v[10:13], v[62:65], 0
	v_mfma_f32_16x16x32_bf16 v[150:153], v[14:17], v[90:93], v[134:137]
	v_mfma_f32_16x16x32_bf16 v[134:137], v[2:5], v[94:97], 0
	v_mfma_f32_16x16x32_bf16 v[154:157], v[6:9], v[114:117], v[134:137]
	v_mfma_f32_16x16x32_bf16 v[134:137], v[10:13], v[94:97], 0
	v_mfma_f32_16x16x32_bf16 v[158:161], v[14:17], v[114:117], v[134:137]
	v_mfma_f32_16x16x32_bf16 v[134:137], v[2:5], v[118:121], 0
	v_mfma_f32_16x16x32_bf16 v[2:5], v[2:5], v[126:129], 0
	v_mfma_f32_16x16x32_bf16 v[162:165], v[6:9], v[122:125], v[134:137]
	v_mfma_f32_16x16x32_bf16 v[2:5], v[6:9], v[130:133], v[2:5]
	v_mfma_f32_16x16x32_bf16 v[6:9], v[10:13], v[126:129], 0
	v_mfma_f32_16x16x32_bf16 v[134:137], v[10:13], v[118:121], 0
	v_mfma_f32_16x16x32_bf16 v[6:9], v[14:17], v[130:133], v[6:9]
	v_mfma_f32_16x16x32_bf16 v[166:169], v[14:17], v[122:125], v[134:137]
	s_setprio 0
	s_setprio 1
	v_mfma_f32_16x16x32_bf16 v[10:13], v[18:21], v[62:65], 0
	v_mfma_f32_16x16x32_bf16 v[170:173], v[22:25], v[90:93], v[10:13]
	v_mfma_f32_16x16x32_bf16 v[10:13], v[26:29], v[62:65], 0
	v_mfma_f32_16x16x32_bf16 v[174:177], v[30:33], v[90:93], v[10:13]
	v_mfma_f32_16x16x32_bf16 v[10:13], v[18:21], v[94:97], 0
	v_mfma_f32_16x16x32_bf16 v[178:181], v[22:25], v[114:117], v[10:13]
	v_mfma_f32_16x16x32_bf16 v[10:13], v[26:29], v[94:97], 0
	v_mfma_f32_16x16x32_bf16 v[184:187], v[30:33], v[114:117], v[10:13]
	v_mfma_f32_16x16x32_bf16 v[10:13], v[18:21], v[118:121], 0
	v_mfma_f32_16x16x32_bf16 v[194:197], v[22:25], v[122:125], v[10:13]
	v_mfma_f32_16x16x32_bf16 v[10:13], v[26:29], v[118:121], 0
	v_mfma_f32_16x16x32_bf16 v[118:121], v[30:33], v[122:125], v[10:13]
	v_mfma_f32_16x16x32_bf16 v[10:13], v[18:21], v[126:129], 0
	v_mfma_f32_16x16x32_bf16 v[200:203], v[22:25], v[130:133], v[10:13]
	v_mfma_f32_16x16x32_bf16 v[10:13], v[26:29], v[126:129], 0
	v_mfma_f32_16x16x32_bf16 v[204:207], v[30:33], v[130:133], v[10:13]
	s_setprio 0
	s_barrier
	s_add_i32 s61, 0, 0x18000
	s_add_i32 s63, 0, 0x1c000
	v_add_u32_e32 v100, s61, v193
	v_add_u32_e32 v101, s63, v193
	s_nop 0
	ds_read_b128 v[10:13], v100
	ds_read_b128 v[14:17], v100 offset:1024
	ds_read_b128 v[18:21], v100 offset:2048
	ds_read_b128 v[22:25], v100 offset:3072
	ds_read_b128 v[214:217], v101
	ds_read_b128 v[218:221], v101 offset:1024
	ds_read_b128 v[222:225], v101 offset:2048
	ds_read_b128 v[226:229], v101 offset:3072
	s_add_u32 s18, s34, 0x40100
	s_addc_u32 s19, s35, 0
	s_mov_b32 m0, s51
	ds_read_b128 v[26:29], v199 offset:32768
	ds_read_b128 v[30:33], v199 offset:33792
	ds_read_b128 v[62:65], v199 offset:34816
	ds_read_b128 v[230:233], v199 offset:35840
	ds_read_b128 v[234:237], v199 offset:36864
	ds_read_b128 v[238:241], v199 offset:37888
	ds_read_b128 v[242:245], v199 offset:38912
	ds_read_b128 v[246:249], v199 offset:39936
	s_nop 0
	v_lshl_add_u64 v[90:91], s[18:19], 0, v[190:191]
	global_load_lds_dwordx4 v[90:91], off
	v_lshl_add_u64 v[90:91], s[18:19], 0, v[182:183]
	s_mov_b32 m0, s52
	s_nop 0
	global_load_lds_dwordx4 v[90:91], off
	s_waitcnt vmcnt(8)
	s_waitcnt lgkmcnt(0)
	s_barrier
	s_setprio 1
	s_waitcnt lgkmcnt(0)
	v_mfma_f32_16x16x32_bf16 v[66:69], v[10:13], v[26:29], v[66:69]
	v_mfma_f32_16x16x32_bf16 v[134:137], v[14:17], v[30:33], v[66:69]
	v_mfma_f32_16x16x32_bf16 v[66:69], v[18:21], v[26:29], v[70:73]
	v_mfma_f32_16x16x32_bf16 v[142:145], v[22:25], v[30:33], v[66:69]
	v_mfma_f32_16x16x32_bf16 v[66:69], v[10:13], v[62:65], v[74:77]
	v_mfma_f32_16x16x32_bf16 v[126:129], v[14:17], v[230:233], v[66:69]
	v_mfma_f32_16x16x32_bf16 v[66:69], v[18:21], v[62:65], v[78:81]
	v_mfma_f32_16x16x32_bf16 v[122:125], v[22:25], v[230:233], v[66:69]
	v_mfma_f32_16x16x32_bf16 v[66:69], v[10:13], v[234:237], v[82:85]
	v_mfma_f32_16x16x32_bf16 v[94:97], v[14:17], v[238:241], v[66:69]
	v_mfma_f32_16x16x32_bf16 v[66:69], v[18:21], v[234:237], v[86:89]
	v_mfma_f32_16x16x32_bf16 v[90:93], v[22:25], v[238:241], v[66:69]
	v_mfma_f32_16x16x32_bf16 v[66:69], v[10:13], v[242:245], v[102:105]
	v_mfma_f32_16x16x32_bf16 v[78:81], v[14:17], v[246:249], v[66:69]
	v_mfma_f32_16x16x32_bf16 v[66:69], v[18:21], v[242:245], v[106:109]
	v_mfma_f32_16x16x32_bf16 v[70:73], v[22:25], v[246:249], v[66:69]
	s_setprio 0
	s_setprio 1
	v_mfma_f32_16x16x32_bf16 v[66:69], v[214:217], v[26:29], v[110:113]
	v_mfma_f32_16x16x32_bf16 v[26:29], v[222:225], v[26:29], v[34:37]
	v_mfma_f32_16x16x32_bf16 v[130:133], v[226:229], v[30:33], v[26:29]
	v_mfma_f32_16x16x32_bf16 v[26:29], v[214:217], v[62:65], v[38:41]
	v_mfma_f32_16x16x32_bf16 v[114:117], v[218:221], v[230:233], v[26:29]
	v_mfma_f32_16x16x32_bf16 v[26:29], v[222:225], v[62:65], v[42:45]
	v_mfma_f32_16x16x32_bf16 v[110:113], v[226:229], v[230:233], v[26:29]
	v_mfma_f32_16x16x32_bf16 v[26:29], v[214:217], v[234:237], v[46:49]
	v_mfma_f32_16x16x32_bf16 v[86:89], v[218:221], v[238:241], v[26:29]
	v_mfma_f32_16x16x32_bf16 v[26:29], v[222:225], v[234:237], v[50:53]
	v_mfma_f32_16x16x32_bf16 v[82:85], v[226:229], v[238:241], v[26:29]
	v_mfma_f32_16x16x32_bf16 v[26:29], v[214:217], v[242:245], v[54:57]
	v_mfma_f32_16x16x32_bf16 v[62:65], v[218:221], v[246:249], v[26:29]
	v_mfma_f32_16x16x32_bf16 v[26:29], v[222:225], v[242:245], v[58:61]
	v_mfma_f32_16x16x32_bf16 v[138:141], v[218:221], v[30:33], v[66:69]
	v_mfma_f32_16x16x32_bf16 v[54:57], v[226:229], v[246:249], v[26:29]
	s_setprio 0
	s_barrier
	s_add_u32 s18, s30, 0x180
	s_addc_u32 s19, s31, 0
	s_add_i32 s61, s61, s48
	ds_read_b128 v[34:37], v199 offset:49152
	ds_read_b128 v[38:41], v199 offset:50176
	ds_read_b128 v[102:105], v199 offset:51200
	ds_read_b128 v[106:109], v199 offset:52224
	ds_read_b128 v[230:233], v199 offset:53248
	ds_read_b128 v[234:237], v199 offset:54272
	ds_read_b128 v[238:241], v199 offset:55296
	ds_read_b128 v[242:245], v199 offset:56320
	s_mov_b32 m0, s61
	v_lshl_add_u64 v[26:27], s[18:19], 0, v[190:191]
	s_add_i32 s62, s61, 0x2000
	global_load_lds_dwordx4 v[26:27], off
	v_lshl_add_u64 v[26:27], s[18:19], 0, v[182:183]
	s_add_u32 s18, s30, 0x40180
	s_mov_b32 m0, s62
	s_addc_u32 s19, s31, 0
	s_add_i32 s63, s63, s48
	global_load_lds_dwordx4 v[26:27], off
	s_mov_b32 m0, s63
	v_lshl_add_u64 v[26:27], s[18:19], 0, v[190:191]
	s_add_i32 s64, s63, 0x2000
	global_load_lds_dwordx4 v[26:27], off
	v_lshl_add_u64 v[26:27], s[18:19], 0, v[182:183]
	s_mov_b32 m0, s64
	s_nop 0
	global_load_lds_dwordx4 v[26:27], off
	s_mov_b32 m0, s53
	v_lshl_add_u64 v[26:27], s[40:41], 0, v[190:191]
	global_load_lds_dwordx4 v[26:27], off
	v_lshl_add_u64 v[26:27], s[40:41], 0, v[182:183]
	s_mov_b32 m0, s54
	s_nop 0
	global_load_lds_dwordx4 v[26:27], off
	s_waitcnt vmcnt(8)
	s_waitcnt lgkmcnt(0)
	s_barrier
	s_setprio 1
	s_waitcnt lgkmcnt(0)
	v_mfma_f32_16x16x32_bf16 v[26:29], v[10:13], v[34:37], v[146:149]
	v_mfma_f32_16x16x32_bf16 v[74:77], v[14:17], v[38:41], v[26:29]
	v_mfma_f32_16x16x32_bf16 v[26:29], v[18:21], v[34:37], v[150:153]
	v_mfma_f32_16x16x32_bf16 v[66:69], v[22:25], v[38:41], v[26:29]
	v_mfma_f32_16x16x32_bf16 v[26:29], v[10:13], v[102:105], v[154:157]
	v_mfma_f32_16x16x32_bf16 v[46:49], v[14:17], v[106:109], v[26:29]
	v_mfma_f32_16x16x32_bf16 v[26:29], v[18:21], v[102:105], v[158:161]
	v_mfma_f32_16x16x32_bf16 v[42:45], v[22:25], v[106:109], v[26:29]
	v_mfma_f32_16x16x32_bf16 v[26:29], v[10:13], v[230:233], v[162:165]
	v_mfma_f32_16x16x32_bf16 v[2:5], v[10:13], v[238:241], v[2:5]
	v_mfma_f32_16x16x32_bf16 v[30:33], v[14:17], v[234:237], v[26:29]
	v_mfma_f32_16x16x32_bf16 v[26:29], v[18:21], v[230:233], v[166:169]
	v_mfma_f32_16x16x32_bf16 v[14:17], v[14:17], v[242:245], v[2:5]
	v_mfma_f32_16x16x32_bf16 v[2:5], v[18:21], v[238:241], v[6:9]
	v_mfma_f32_16x16x32_bf16 v[26:29], v[22:25], v[234:237], v[26:29]
	v_mfma_f32_16x16x32_bf16 v[10:13], v[22:25], v[242:245], v[2:5]
	s_setprio 0
	s_setprio 1
	v_mfma_f32_16x16x32_bf16 v[2:5], v[214:217], v[34:37], v[170:173]
	v_mfma_f32_16x16x32_bf16 v[58:61], v[218:221], v[38:41], v[2:5]
	v_mfma_f32_16x16x32_bf16 v[2:5], v[222:225], v[34:37], v[174:177]
	v_mfma_f32_16x16x32_bf16 v[50:53], v[226:229], v[38:41], v[2:5]
	v_mfma_f32_16x16x32_bf16 v[2:5], v[214:217], v[102:105], v[178:181]
	v_mfma_f32_16x16x32_bf16 v[38:41], v[218:221], v[106:109], v[2:5]
	v_mfma_f32_16x16x32_bf16 v[2:5], v[222:225], v[102:105], v[184:187]
	v_mfma_f32_16x16x32_bf16 v[34:37], v[226:229], v[106:109], v[2:5]
	v_mfma_f32_16x16x32_bf16 v[2:5], v[214:217], v[230:233], v[194:197]
	v_mfma_f32_16x16x32_bf16 v[22:25], v[218:221], v[234:237], v[2:5]
	v_mfma_f32_16x16x32_bf16 v[2:5], v[222:225], v[230:233], v[118:121]
	v_mfma_f32_16x16x32_bf16 v[18:21], v[226:229], v[234:237], v[2:5]
	v_mfma_f32_16x16x32_bf16 v[2:5], v[214:217], v[238:241], v[200:203]
	v_mfma_f32_16x16x32_bf16 v[6:9], v[218:221], v[242:245], v[2:5]
	v_mfma_f32_16x16x32_bf16 v[2:5], v[222:225], v[238:241], v[204:207]
	v_mfma_f32_16x16x32_bf16 v[2:5], v[226:229], v[242:245], v[2:5]
	s_setprio 0
	s_barrier
	s_mov_b32 s65, 0

; #define PG8_STAGE(bufoff, gbase, voff) do { const char* gb_ = (const char*)(gbase); asm volatile("" : "+s"(gb_));     \
;         _Pragma("unroll") for (int _i = 0; _i < 2; ++_i) \
;         __builtin_amdgcn_global_load_lds((const unsigned*)(gb_ + (voff)[_i]), (LAS unsigned*)(lds + (bufoff) + ldsw + _i * 8192), 16, 0, 0); } while (0)
; #define PG8_STAGE_A(bufoff, gbase, h, vo) do { if constexpr (GATHER) { PG8_STAGE(bufoff, gbase, (vo)[h]); } else { PG8_STAGE(bufoff, (gbase) + (h) * hstep, voffA); } } while (0)
; #define PG8_WAIT_V(n) asm volatile("s_waitcnt vmcnt(" #n ")" ::: "memory")
; #define PG8_BAR __builtin_amdgcn_s_barrier()
;     ...
;     const int aoff = lds_byte(wr * 64 + fr, fq * 8), boff = lds_byte(wc * 32 + fr, fq * 8);
;     ...
;     if constexpr (SP2) {
;         PG8_STAGE(PG8_SB(0, 0), cB + PG8_KO(0), voffB); PG8_STAGE(PG8_SB(0, 1), cB + hstep + PG8_KO(0), voffB); PG8_STAGE_A(PG8_SA(0, 0), cA + PG8_KO(0), 0, cvo); PG8_STAGE_A(PG8_SA(0, 1), cA + PG8_KO(0), 1, cvo);
;         if (wr == 1) PG8_BAR;
;         PG8_WAIT_V(2); PG8_BAR;
;         PG8_STAGE(PG8_SB(1, 0), cB + PG8_KO(1), voffB); PG8_STAGE_A(PG8_SA(1, 0), cA + PG8_KO(1), 0, cvo); PG8_STAGE(PG8_SB(1, 1), cB + hstep + PG8_KO(1), voffB);
;         PG8_WAIT_V(6); PG8_BAR;
.LBB0_1076:
	v_lshrrev_b32_e32 v4, 1, v2
	v_and_b32_e32 v4, 24, v4
	v_and_b32_e32 v3, 15, v2
	v_lshlrev_b32_e32 v5, 1, v4
	v_lshlrev_b32_e32 v2, 2, v2
	v_lshl_or_b32 v1, s10, 6, v3
	v_lshl_or_b32 v3, v3, 6, v5
	s_lshl_b32 s3, s10, 13
	v_and_b32_e32 v2, 32, v2
	v_bitop3_b32 v5, v3, s3, v2 bitop3:0xde
	s_lshl_b32 s3, s5, 5
	s_and_b32 s3, s3, 0x60
	s_lshl_b32 s5, s3, 7
	s_add_u32 s10, s8, 0x80
	s_addc_u32 s11, s9, 0
	v_bitop3_b32 v193, v3, s5, v2 bitop3:0xde
	s_waitcnt vmcnt(2)
	s_barrier
	s_add_i32 m0, s7, 0x18000
	v_lshl_add_u64 v[2:3], s[10:11], 0, v[190:191]
	v_mov_b32_e32 v179, v191
	global_load_lds_dwordx4 v[2:3], off
	s_add_i32 m0, s7, 0x1a000
	v_lshl_add_u64 v[2:3], s[10:11], 0, v[178:179]
	s_add_u32 s10, s28, 0x80
	s_addc_u32 s11, s29, 0
	s_add_i32 s55, s7, 0x8000
	global_load_lds_dwordx4 v[2:3], off
	s_mov_b32 m0, s55
	v_lshl_add_u64 v[2:3], s[10:11], 0, v[190:191]
	s_add_i32 s56, s7, 0xa000
	global_load_lds_dwordx4 v[2:3], off
	v_lshl_add_u64 v[2:3], s[10:11], 0, v[178:179]
	s_add_u32 s10, s8, 0x20080
	s_mov_b32 m0, s56
	s_addc_u32 s11, s9, 0
	global_load_lds_dwordx4 v[2:3], off
	s_add_i32 m0, s7, 0x1c000
	v_lshl_add_u64 v[2:3], s[10:11], 0, v[190:191]
	global_load_lds_dwordx4 v[2:3], off
	v_lshl_add_u64 v[2:3], s[10:11], 0, v[178:179]
	s_add_i32 m0, s7, 0x1e000
	s_cmpk_lt_u32 s4, 0x100
	global_load_lds_dwordx4 v[2:3], off
	s_waitcnt vmcnt(0)
	s_cselect_b64 s[4:5], -1, 0
	v_or_b32_e32 v214, s3, v4
	s_mov_b32 s57, 0
	v_add_u32_e32 v215, 0, v5
	s_barrier
	s_branch .LBB0_1079

.LBB0_1081:
	s_ashr_i32 s23, s22, 31
	s_lshl_b64 s[18:19], s[22:23], 18
	s_add_u32 s34, s96, s18
	s_addc_u32 s35, s97, s19
	s_ashr_i32 s11, s10, 31
	s_lshl_b64 s[18:19], s[10:11], 18
	s_add_u32 s38, s17, s18
	s_addc_u32 s39, s25, s19
	s_add_u32 s18, s28, 0x100
	s_addc_u32 s19, s29, 0
	s_add_u32 s40, s28, 0x180
	s_addc_u32 s41, s29, 0
	s_add_u32 s42, s8, 0x100
	s_addc_u32 s43, s9, 0
	s_add_i32 s23, 0, 0x10000
	s_add_i32 s59, 0, 0x14000
	v_add_u32_e32 v162, s23, v193
	v_add_u32_e32 v163, s59, v193
	ds_read_b128 v[2:5], v162
	ds_read_b128 v[6:9], v162 offset:1024
	ds_read_b128 v[10:13], v162 offset:2048
	ds_read_b128 v[14:17], v162 offset:3072
	ds_read_b128 v[18:21], v163
	ds_read_b128 v[22:25], v163 offset:1024
	ds_read_b128 v[26:29], v163 offset:2048
	ds_read_b128 v[30:33], v163 offset:3072
	s_mov_b64 s[30:31], 0x100
	s_add_u32 s44, s28, 0x20080
	s_addc_u32 s45, s29, 0
	s_add_i32 s3, s7, 0xc000
	ds_read_b128 v[34:37], v215
	ds_read_b128 v[38:41], v215 offset:1024
	ds_read_b128 v[42:45], v215 offset:2048
	ds_read_b128 v[46:49], v215 offset:3072
	ds_read_b128 v[50:53], v215 offset:4096
	ds_read_b128 v[54:57], v215 offset:5120
	ds_read_b128 v[58:61], v215 offset:6144
	ds_read_b128 v[62:65], v215 offset:7168
	s_mov_b32 m0, s3
	v_lshl_add_u64 v[66:67], s[44:45], 0, v[190:191]
	s_add_i32 s11, s7, 0xe000
	global_load_lds_dwordx4 v[66:67], off
	v_lshl_add_u64 v[66:67], s[44:45], 0, v[178:179]
	s_mov_b32 m0, s11
	s_nop 0
	global_load_lds_dwordx4 v[66:67], off
	s_waitcnt vmcnt(24)
	s_waitcnt lgkmcnt(0)
	s_barrier
	s_setprio 1
	s_waitcnt lgkmcnt(0)
	v_mfma_f32_16x16x128_f8f6f4 v[146:149], v[2:9], v[34:41], 0
	v_mfma_f32_16x16x128_f8f6f4 v[150:153], v[10:17], v[34:41], 0
	v_mfma_f32_16x16x128_f8f6f4 v[138:141], v[2:9], v[42:49], 0
	v_mfma_f32_16x16x128_f8f6f4 v[130:133], v[10:17], v[42:49], 0
	v_mfma_f32_16x16x128_f8f6f4 v[126:129], v[2:9], v[50:57], 0
	v_mfma_f32_16x16x128_f8f6f4 v[118:121], v[10:17], v[50:57], 0
	v_mfma_f32_16x16x128_f8f6f4 v[106:109], v[2:9], v[58:65], 0
	v_mfma_f32_16x16x128_f8f6f4 v[94:97], v[10:17], v[58:65], 0
	s_setprio 0
	s_setprio 1
	v_mfma_f32_16x16x128_f8f6f4 v[154:157], v[18:25], v[34:41], 0
	v_mfma_f32_16x16x128_f8f6f4 v[158:161], v[26:33], v[34:41], 0
	v_mfma_f32_16x16x128_f8f6f4 v[142:145], v[18:25], v[42:49], 0
	v_mfma_f32_16x16x128_f8f6f4 v[134:137], v[26:33], v[42:49], 0
	v_mfma_f32_16x16x128_f8f6f4 v[122:125], v[18:25], v[50:57], 0
	v_mfma_f32_16x16x128_f8f6f4 v[114:117], v[26:33], v[50:57], 0
	v_mfma_f32_16x16x128_f8f6f4 v[86:89], v[18:25], v[58:65], 0
	v_mfma_f32_16x16x128_f8f6f4 v[82:85], v[26:33], v[58:65], 0
	s_setprio 0
	s_barrier
	s_add_i32 s23, s23, s33
	ds_read_b128 v[34:37], v215 offset:16384
	ds_read_b128 v[38:41], v215 offset:17408
	ds_read_b128 v[50:53], v215 offset:18432
	ds_read_b128 v[54:57], v215 offset:19456
	ds_read_b128 v[164:167], v215 offset:20480
	ds_read_b128 v[168:171], v215 offset:21504
	ds_read_b128 v[180:183], v215 offset:22528
	ds_read_b128 v[184:187], v215 offset:23552
	s_mov_b32 m0, s23
	v_lshl_add_u64 v[42:43], s[42:43], 0, v[190:191]
	s_add_i32 s58, s23, 0x2000
	global_load_lds_dwordx4 v[42:43], off
	v_lshl_add_u64 v[42:43], s[42:43], 0, v[178:179]
	s_add_u32 s42, s8, 0x20100
	s_mov_b32 m0, s58
	s_addc_u32 s43, s9, 0
	s_add_i32 s59, s59, s33
	global_load_lds_dwordx4 v[42:43], off
	s_mov_b32 m0, s59
	v_lshl_add_u64 v[42:43], s[42:43], 0, v[190:191]
	s_add_i32 s61, s59, 0x2000
	global_load_lds_dwordx4 v[42:43], off
	v_lshl_add_u64 v[42:43], s[42:43], 0, v[178:179]
	s_mov_b32 m0, s61
	s_nop 0
	global_load_lds_dwordx4 v[42:43], off
	s_mov_b32 m0, s7
	v_lshl_add_u64 v[42:43], s[18:19], 0, v[190:191]
	global_load_lds_dwordx4 v[42:43], off
	v_lshl_add_u64 v[42:43], s[18:19], 0, v[178:179]
	s_mov_b32 m0, s52
	s_nop 0
	global_load_lds_dwordx4 v[42:43], off
	s_waitcnt vmcnt(24)
	s_waitcnt lgkmcnt(0)
	s_barrier
	s_setprio 1
	s_waitcnt lgkmcnt(0)
	v_mfma_f32_16x16x128_f8f6f4 v[110:113], v[2:9], v[34:41], 0
	v_mfma_f32_16x16x128_f8f6f4 v[98:101], v[10:17], v[34:41], 0
	v_mfma_f32_16x16x128_f8f6f4 v[78:81], v[2:9], v[50:57], 0
	v_mfma_f32_16x16x128_f8f6f4 v[74:77], v[10:17], v[50:57], 0
	v_mfma_f32_16x16x128_f8f6f4 v[62:65], v[2:9], v[164:171], 0
	v_mfma_f32_16x16x128_f8f6f4 v[58:61], v[10:17], v[164:171], 0
	v_mfma_f32_16x16x128_f8f6f4 v[46:49], v[2:9], v[180:187], 0
	v_mfma_f32_16x16x128_f8f6f4 v[42:45], v[10:17], v[180:187], 0
	s_setprio 0
	s_setprio 1
	v_mfma_f32_16x16x128_f8f6f4 v[102:105], v[18:25], v[34:41], 0
	v_mfma_f32_16x16x128_f8f6f4 v[90:93], v[26:33], v[34:41], 0
	v_mfma_f32_16x16x128_f8f6f4 v[70:73], v[18:25], v[50:57], 0
	v_mfma_f32_16x16x128_f8f6f4 v[66:69], v[26:33], v[50:57], 0
	v_mfma_f32_16x16x128_f8f6f4 v[54:57], v[18:25], v[164:171], 0
	v_mfma_f32_16x16x128_f8f6f4 v[50:53], v[26:33], v[164:171], 0
	v_mfma_f32_16x16x128_f8f6f4 v[38:41], v[18:25], v[180:187], 0
	v_mfma_f32_16x16x128_f8f6f4 v[34:37], v[26:33], v[180:187], 0
	s_setprio 0
	s_barrier
	s_add_i32 s44, 0, 0x18000
	s_add_i32 s62, 0, 0x1c000
	v_add_u32_e32 v164, s44, v193
	v_add_u32_e32 v165, s62, v193
	ds_read_b128 v[26:29], v164
	ds_read_b128 v[30:33], v164 offset:1024
	ds_read_b128 v[18:21], v164 offset:2048
	ds_read_b128 v[22:25], v164 offset:3072
	ds_read_b128 v[10:13], v165
	ds_read_b128 v[14:17], v165 offset:1024
	ds_read_b128 v[2:5], v165 offset:2048
	ds_read_b128 v[6:9], v165 offset:3072
	s_add_u32 s18, s28, 0x20100
	s_addc_u32 s19, s29, 0
	s_mov_b32 m0, s53
	ds_read_b128 v[166:169], v215 offset:32768
	ds_read_b128 v[170:173], v215 offset:33792
	ds_read_b128 v[180:183], v215 offset:34816
	ds_read_b128 v[184:187], v215 offset:35840
	ds_read_b128 v[194:197], v215 offset:36864
	ds_read_b128 v[198:201], v215 offset:37888
	ds_read_b128 v[216:219], v215 offset:38912
	ds_read_b128 v[220:223], v215 offset:39936
	s_nop 0
	v_lshl_add_u64 v[174:175], s[18:19], 0, v[190:191]
	global_load_lds_dwordx4 v[174:175], off
	v_lshl_add_u64 v[174:175], s[18:19], 0, v[178:179]
	s_mov_b32 m0, s54
	s_nop 0
	global_load_lds_dwordx4 v[174:175], off
	s_waitcnt vmcnt(8)
	s_waitcnt lgkmcnt(0)
	s_barrier
	s_setprio 1
	s_waitcnt lgkmcnt(0)
	v_mfma_f32_16x16x128_f8f6f4 v[146:149], v[26:33], v[166:173], v[146:149]
	v_mfma_f32_16x16x128_f8f6f4 v[150:153], v[18:25], v[166:173], v[150:153]
	v_mfma_f32_16x16x128_f8f6f4 v[138:141], v[26:33], v[180:187], v[138:141]
	v_mfma_f32_16x16x128_f8f6f4 v[130:133], v[18:25], v[180:187], v[130:133]
	v_mfma_f32_16x16x128_f8f6f4 v[126:129], v[26:33], v[194:201], v[126:129]
	v_mfma_f32_16x16x128_f8f6f4 v[118:121], v[18:25], v[194:201], v[118:121]
	v_mfma_f32_16x16x128_f8f6f4 v[106:109], v[26:33], v[216:223], v[106:109]
	v_mfma_f32_16x16x128_f8f6f4 v[94:97], v[18:25], v[216:223], v[94:97]
	s_setprio 0
	s_setprio 1
	v_mfma_f32_16x16x128_f8f6f4 v[154:157], v[10:17], v[166:173], v[154:157]
	v_mfma_f32_16x16x128_f8f6f4 v[158:161], v[2:9], v[166:173], v[158:161]
	v_mfma_f32_16x16x128_f8f6f4 v[142:145], v[10:17], v[180:187], v[142:145]
	v_mfma_f32_16x16x128_f8f6f4 v[134:137], v[2:9], v[180:187], v[134:137]
	v_mfma_f32_16x16x128_f8f6f4 v[122:125], v[10:17], v[194:201], v[122:125]
	v_mfma_f32_16x16x128_f8f6f4 v[114:117], v[2:9], v[194:201], v[114:117]
	v_mfma_f32_16x16x128_f8f6f4 v[86:89], v[10:17], v[216:223], v[86:89]
	v_mfma_f32_16x16x128_f8f6f4 v[82:85], v[2:9], v[216:223], v[82:85]
	s_setprio 0
	s_barrier
	s_add_u32 s42, s8, 0x180
	s_addc_u32 s43, s9, 0
	s_add_i32 s18, s44, s33
	ds_read_b128 v[166:169], v215 offset:49152
	ds_read_b128 v[170:173], v215 offset:50176
	ds_read_b128 v[180:183], v215 offset:51200
	ds_read_b128 v[184:187], v215 offset:52224
	ds_read_b128 v[194:197], v215 offset:53248
	ds_read_b128 v[198:201], v215 offset:54272
	ds_read_b128 v[216:219], v215 offset:55296
	ds_read_b128 v[220:223], v215 offset:56320
	s_mov_b32 m0, s18
	v_lshl_add_u64 v[174:175], s[42:43], 0, v[190:191]
	s_add_i32 s19, s18, 0x2000
	global_load_lds_dwordx4 v[174:175], off
	v_lshl_add_u64 v[174:175], s[42:43], 0, v[178:179]
	s_add_u32 s42, s8, 0x20180
	s_mov_b32 m0, s19
	s_addc_u32 s43, s9, 0
	s_add_i32 s62, s62, s33
	global_load_lds_dwordx4 v[174:175], off
	s_mov_b32 m0, s62
	v_lshl_add_u64 v[174:175], s[42:43], 0, v[190:191]
	s_add_i32 s63, s62, 0x2000
	global_load_lds_dwordx4 v[174:175], off
	v_lshl_add_u64 v[174:175], s[42:43], 0, v[178:179]
	s_mov_b32 m0, s63
	s_nop 0
	global_load_lds_dwordx4 v[174:175], off
	s_mov_b32 m0, s55
	v_lshl_add_u64 v[174:175], s[40:41], 0, v[190:191]
	global_load_lds_dwordx4 v[174:175], off
	v_lshl_add_u64 v[174:175], s[40:41], 0, v[178:179]
	s_mov_b32 m0, s56
	s_nop 0
	global_load_lds_dwordx4 v[174:175], off
	s_waitcnt vmcnt(8)
	s_waitcnt lgkmcnt(0)
	s_barrier
	s_setprio 1
	s_waitcnt lgkmcnt(0)
	v_mfma_f32_16x16x128_f8f6f4 v[110:113], v[26:33], v[166:173], v[110:113]
	v_mfma_f32_16x16x128_f8f6f4 v[98:101], v[18:25], v[166:173], v[98:101]
	v_mfma_f32_16x16x128_f8f6f4 v[78:81], v[26:33], v[180:187], v[78:81]
	v_mfma_f32_16x16x128_f8f6f4 v[74:77], v[18:25], v[180:187], v[74:77]
	v_mfma_f32_16x16x128_f8f6f4 v[62:65], v[26:33], v[194:201], v[62:65]
	v_mfma_f32_16x16x128_f8f6f4 v[58:61], v[18:25], v[194:201], v[58:61]
	v_mfma_f32_16x16x128_f8f6f4 v[46:49], v[26:33], v[216:223], v[46:49]
	v_mfma_f32_16x16x128_f8f6f4 v[42:45], v[18:25], v[216:223], v[42:45]
	s_setprio 0
	s_setprio 1
	v_mfma_f32_16x16x128_f8f6f4 v[102:105], v[10:17], v[166:173], v[102:105]
	v_mfma_f32_16x16x128_f8f6f4 v[90:93], v[2:9], v[166:173], v[90:93]
	v_mfma_f32_16x16x128_f8f6f4 v[70:73], v[10:17], v[180:187], v[70:73]
	v_mfma_f32_16x16x128_f8f6f4 v[66:69], v[2:9], v[180:187], v[66:69]
	v_mfma_f32_16x16x128_f8f6f4 v[54:57], v[10:17], v[194:201], v[54:57]
	v_mfma_f32_16x16x128_f8f6f4 v[50:53], v[2:9], v[194:201], v[50:53]
	v_mfma_f32_16x16x128_f8f6f4 v[38:41], v[10:17], v[216:223], v[38:41]
	v_mfma_f32_16x16x128_f8f6f4 v[34:37], v[2:9], v[216:223], v[34:37]
	s_setprio 0
	s_barrier
	s_mov_b32 s64, 0

; #define PG8_STAGE(bufoff, gbase, voff) do { const char* gb_ = (const char*)(gbase); asm volatile("" : "+s"(gb_));     \
;         _Pragma("unroll") for (int _i = 0; _i < 2; ++_i) \
;         __builtin_amdgcn_global_load_lds((const unsigned*)(gb_ + (voff)[_i]), (LAS unsigned*)(lds + (bufoff) + ldsw + _i * 8192), 16, 0, 0); } while (0)
; #define PG8_STAGE_A(bufoff, gbase, h, vo) do { if constexpr (GATHER) { PG8_STAGE(bufoff, gbase, (vo)[h]); } else { PG8_STAGE(bufoff, (gbase) + (h) * hstep, voffA); } } while (0)
; #define PG8_WAIT_V(n) asm volatile("s_waitcnt vmcnt(" #n ")" ::: "memory")
; #define PG8_BAR __builtin_amdgcn_s_barrier()
;     ...
;     const int aoff = lds_byte(wr * 64 + fr, fq * 8), boff = lds_byte(wc * 32 + fr, fq * 8);
;     ...
;     if constexpr (SP2) {
;         PG8_STAGE(PG8_SB(0, 0), cB + PG8_KO(0), voffB); PG8_STAGE(PG8_SB(0, 1), cB + hstep + PG8_KO(0), voffB); PG8_STAGE_A(PG8_SA(0, 0), cA + PG8_KO(0), 0, cvo); PG8_STAGE_A(PG8_SA(0, 1), cA + PG8_KO(0), 1, cvo);
;         if (wr == 1) PG8_BAR;
;         PG8_WAIT_V(2); PG8_BAR;
;         PG8_STAGE(PG8_SB(1, 0), cB + PG8_KO(1), voffB); PG8_STAGE_A(PG8_SA(1, 0), cA + PG8_KO(1), 0, cvo); PG8_STAGE(PG8_SB(1, 1), cB + hstep + PG8_KO(1), voffB);
;         PG8_WAIT_V(6); PG8_BAR;
.LBB0_1412:
	v_lshrrev_b32_e32 v4, 1, v2
	v_and_b32_e32 v4, 24, v4
	v_and_b32_e32 v3, 15, v2
	v_lshlrev_b32_e32 v5, 1, v4
	v_lshlrev_b32_e32 v2, 2, v2
	v_lshl_or_b32 v175, s3, 6, v3
	v_lshl_or_b32 v3, v3, 6, v5
	s_lshl_b32 s3, s3, 13
	v_and_b32_e32 v2, 32, v2
	v_bitop3_b32 v5, v3, s3, v2 bitop3:0xde
	s_lshl_b32 s3, s6, 5
	s_and_b32 s8, s3, 0x60
	s_lshl_b32 s3, s8, 7
	s_add_u32 s6, s10, 0x80
	v_mov_b32_e32 v165, v191
	s_addc_u32 s7, s11, 0
	v_mov_b32_e32 v163, v191
	v_bitop3_b32 v176, v3, s3, v2 bitop3:0xde
	s_waitcnt vmcnt(2)
	s_barrier
	s_add_i32 m0, s40, 0x18000
	v_lshl_add_u64 v[2:3], s[6:7], 0, v[164:165]
	global_load_lds_dwordx4 v[2:3], off
	v_lshl_add_u64 v[2:3], s[6:7], 0, v[162:163]
	v_readlane_b32 s6, v254, 11
	v_mov_b32_e32 v171, v191
	s_add_i32 m0, s40, 0x1a000
	v_readlane_b32 s7, v254, 12
	s_add_i32 s44, s40, 0x8000
	v_mov_b32_e32 v169, v191
	global_load_lds_dwordx4 v[2:3], off
	s_mov_b32 m0, s44
	v_lshl_add_u64 v[2:3], s[6:7], 0, v[170:171]
	s_add_i32 s45, s40, 0xa000
	global_load_lds_dwordx4 v[2:3], off
	v_lshl_add_u64 v[2:3], s[6:7], 0, v[168:169]
	s_add_u32 s6, s10, 0x20080
	s_mov_b32 m0, s45
	s_addc_u32 s7, s11, 0
	global_load_lds_dwordx4 v[2:3], off
	s_add_i32 m0, s40, 0x1c000
	v_lshl_add_u64 v[2:3], s[6:7], 0, v[164:165]
	global_load_lds_dwordx4 v[2:3], off
	v_lshl_add_u64 v[2:3], s[6:7], 0, v[162:163]
	s_add_i32 m0, s40, 0x1e000
	s_cmpk_lt_u32 s2, 0x100
	global_load_lds_dwordx4 v[2:3], off
	s_waitcnt vmcnt(0)
	v_readlane_b32 s6, v254, 30
	s_cselect_b64 s[2:3], -1, 0
	v_or_b32_e32 v169, s8, v4
	s_mov_b32 s48, 0
	v_add_u32_e32 v171, 0, v5
	s_mov_b32 s50, s6
	v_readlane_b32 s51, v254, 28
	s_barrier
	v_readlane_b32 s7, v254, 31
	s_branch .LBB0_1415

.LBB0_1423:
	s_ashr_i32 s7, s6, 31
	s_lshl_b64 s[8:9], s[6:7], 18
	s_add_u32 s8, s17, s8
	s_addc_u32 s9, s25, s9
	s_add_u32 s18, s10, 0x100
	s_addc_u32 s19, s11, 0
	s_add_i32 s53, 0, 0x10000
	s_add_i32 s30, 0, 0x14000
	v_add_u32_e32 v181, s53, v176
	v_add_u32_e32 v182, s30, v176
	ds_read_b128 v[2:5], v181
	ds_read_b128 v[6:9], v181 offset:1024
	ds_read_b128 v[10:13], v181 offset:2048
	ds_read_b128 v[14:17], v181 offset:3072
	ds_read_b128 v[18:21], v182
	ds_read_b128 v[22:25], v182 offset:1024
	ds_read_b128 v[26:29], v182 offset:2048
	ds_read_b128 v[30:33], v182 offset:3072
	v_readlane_b32 s28, v254, 11
	s_add_i32 s7, s40, 0xc000
	v_readlane_b32 s29, v254, 12
	s_mov_b32 m0, s7
	s_add_i32 s52, s40, 0xe000
	ds_read_b128 v[34:37], v171
	ds_read_b128 v[38:41], v171 offset:1024
	ds_read_b128 v[42:45], v171 offset:2048
	ds_read_b128 v[46:49], v171 offset:3072
	ds_read_b128 v[50:53], v171 offset:4096
	ds_read_b128 v[54:57], v171 offset:5120
	ds_read_b128 v[58:61], v171 offset:6144
	ds_read_b128 v[62:65], v171 offset:7168
	v_mov_b32_e32 v167, v191
	global_load_lds_dwordx4 v190, s[28:29]
	s_mov_b32 m0, s52
	s_nop 0
	global_load_lds_dwordx4 v166, s[28:29]
	s_waitcnt vmcnt(16)
	s_waitcnt lgkmcnt(0)
	s_barrier
	s_setprio 1
	s_waitcnt lgkmcnt(0)
	v_mfma_f32_16x16x128_f8f6f4 v[150:153], v[2:9], v[34:41], 0
	v_mfma_f32_16x16x128_f8f6f4 v[146:149], v[10:17], v[34:41], 0
	v_mfma_f32_16x16x128_f8f6f4 v[134:137], v[2:9], v[42:49], 0
	v_mfma_f32_16x16x128_f8f6f4 v[130:133], v[10:17], v[42:49], 0
	v_mfma_f32_16x16x128_f8f6f4 v[118:121], v[2:9], v[50:57], 0
	v_mfma_f32_16x16x128_f8f6f4 v[114:117], v[10:17], v[50:57], 0
	v_mfma_f32_16x16x128_f8f6f4 v[90:93], v[2:9], v[58:65], 0
	v_mfma_f32_16x16x128_f8f6f4 v[82:85], v[10:17], v[58:65], 0
	s_setprio 0
	s_setprio 1
	v_mfma_f32_16x16x128_f8f6f4 v[158:161], v[18:25], v[34:41], 0
	v_mfma_f32_16x16x128_f8f6f4 v[154:157], v[26:33], v[34:41], 0
	v_mfma_f32_16x16x128_f8f6f4 v[142:145], v[18:25], v[42:49], 0
	v_mfma_f32_16x16x128_f8f6f4 v[138:141], v[26:33], v[42:49], 0
	v_mfma_f32_16x16x128_f8f6f4 v[126:129], v[18:25], v[50:57], 0
	v_mfma_f32_16x16x128_f8f6f4 v[122:125], v[26:33], v[50:57], 0
	v_mfma_f32_16x16x128_f8f6f4 v[102:105], v[18:25], v[58:65], 0
	v_mfma_f32_16x16x128_f8f6f4 v[98:101], v[26:33], v[58:65], 0
	s_setprio 0
	s_barrier
	s_add_i32 s53, s53, s33
	ds_read_b128 v[42:45], v171 offset:16384
	ds_read_b128 v[46:49], v171 offset:17408
	ds_read_b128 v[58:61], v171 offset:18432
	ds_read_b128 v[62:65], v171 offset:19456
	ds_read_b128 v[194:197], v171 offset:20480
	ds_read_b128 v[198:201], v171 offset:21504
	ds_read_b128 v[214:217], v171 offset:22528
	ds_read_b128 v[218:221], v171 offset:23552
	s_mov_b32 m0, s53
	v_lshl_add_u64 v[34:35], s[18:19], 0, v[164:165]
	global_load_lds_dwordx4 v[34:35], off
	v_lshl_add_u64 v[34:35], s[18:19], 0, v[162:163]
	s_add_i32 s18, s53, 0x2000
	s_add_u32 s28, s10, 0x20100
	s_mov_b32 m0, s18
	s_addc_u32 s29, s11, 0
	s_add_i32 s19, s30, s33
	global_load_lds_dwordx4 v[34:35], off
	s_mov_b32 m0, s19
	v_lshl_add_u64 v[34:35], s[28:29], 0, v[164:165]
	s_add_i32 s54, s19, 0x2000
	v_readlane_b32 s30, v254, 13
	global_load_lds_dwordx4 v[34:35], off
	v_lshl_add_u64 v[34:35], s[28:29], 0, v[162:163]
	s_mov_b32 m0, s54
	v_readlane_b32 s31, v254, 14
	global_load_lds_dwordx4 v[34:35], off
	s_mov_b64 s[28:29], s[30:31]
	s_mov_b32 m0, s40
	s_nop 0
	global_load_lds_dwordx4 v170, s[28:29]
	s_mov_b32 m0, s41
	s_nop 0
	global_load_lds_dwordx4 v168, s[28:29]
	s_waitcnt vmcnt(16)
	s_waitcnt lgkmcnt(0)
	s_barrier
	s_setprio 1
	s_waitcnt lgkmcnt(0)
	v_mfma_f32_16x16x128_f8f6f4 v[94:97], v[2:9], v[42:49], 0
	v_mfma_f32_16x16x128_f8f6f4 v[86:89], v[10:17], v[42:49], 0
	v_mfma_f32_16x16x128_f8f6f4 v[70:73], v[2:9], v[58:65], 0
	v_mfma_f32_16x16x128_f8f6f4 v[66:69], v[10:17], v[58:65], 0
	v_mfma_f32_16x16x128_f8f6f4 v[54:57], v[2:9], v[194:201], 0
	v_mfma_f32_16x16x128_f8f6f4 v[50:53], v[10:17], v[194:201], 0
	v_mfma_f32_16x16x128_f8f6f4 v[38:41], v[2:9], v[214:221], 0
	v_mfma_f32_16x16x128_f8f6f4 v[34:37], v[10:17], v[214:221], 0
	s_setprio 0
	s_setprio 1
	v_mfma_f32_16x16x128_f8f6f4 v[110:113], v[18:25], v[42:49], 0
	v_mfma_f32_16x16x128_f8f6f4 v[106:109], v[26:33], v[42:49], 0
	v_mfma_f32_16x16x128_f8f6f4 v[78:81], v[18:25], v[58:65], 0
	v_mfma_f32_16x16x128_f8f6f4 v[74:77], v[26:33], v[58:65], 0
	v_mfma_f32_16x16x128_f8f6f4 v[62:65], v[18:25], v[194:201], 0
	v_mfma_f32_16x16x128_f8f6f4 v[58:61], v[26:33], v[194:201], 0
	v_mfma_f32_16x16x128_f8f6f4 v[46:49], v[18:25], v[214:221], 0
	v_mfma_f32_16x16x128_f8f6f4 v[42:45], v[26:33], v[214:221], 0
	s_setprio 0
	s_barrier
	s_add_i32 s55, 0, 0x18000
	s_add_i32 s57, 0, 0x1c000
	v_add_u32_e32 v183, s55, v176
	v_add_u32_e32 v184, s57, v176
	ds_read_b128 v[26:29], v183
	ds_read_b128 v[30:33], v183 offset:1024
	ds_read_b128 v[18:21], v183 offset:2048
	ds_read_b128 v[22:25], v183 offset:3072
	ds_read_b128 v[10:13], v184
	ds_read_b128 v[14:17], v184 offset:1024
	ds_read_b128 v[2:5], v184 offset:2048
	ds_read_b128 v[6:9], v184 offset:3072
	s_mov_b64 s[28:29], s[30:31]
	s_mov_b32 m0, s42
	ds_read_b128 v[194:197], v171 offset:32768
	ds_read_b128 v[198:201], v171 offset:33792
	ds_read_b128 v[214:217], v171 offset:34816
	ds_read_b128 v[218:221], v171 offset:35840
	ds_read_b128 v[222:225], v171 offset:36864
	ds_read_b128 v[226:229], v171 offset:37888
	ds_read_b128 v[230:233], v171 offset:38912
	ds_read_b128 v[234:237], v171 offset:39936
	s_nop 0
	global_load_lds_dwordx4 v190, s[28:29]
	s_mov_b32 m0, s43
	s_nop 0
	global_load_lds_dwordx4 v166, s[28:29]
	s_waitcnt vmcnt(8)
	s_waitcnt lgkmcnt(0)
	s_barrier
	s_setprio 1
	s_waitcnt lgkmcnt(0)
	v_mfma_f32_16x16x128_f8f6f4 v[150:153], v[26:33], v[194:201], v[150:153]
	v_mfma_f32_16x16x128_f8f6f4 v[146:149], v[18:25], v[194:201], v[146:149]
	v_mfma_f32_16x16x128_f8f6f4 v[134:137], v[26:33], v[214:221], v[134:137]
	v_mfma_f32_16x16x128_f8f6f4 v[130:133], v[18:25], v[214:221], v[130:133]
	v_mfma_f32_16x16x128_f8f6f4 v[118:121], v[26:33], v[222:229], v[118:121]
	v_mfma_f32_16x16x128_f8f6f4 v[114:117], v[18:25], v[222:229], v[114:117]
	v_mfma_f32_16x16x128_f8f6f4 v[90:93], v[26:33], v[230:237], v[90:93]
	v_mfma_f32_16x16x128_f8f6f4 v[82:85], v[18:25], v[230:237], v[82:85]
	s_setprio 0
	s_setprio 1
	v_mfma_f32_16x16x128_f8f6f4 v[158:161], v[10:17], v[194:201], v[158:161]
	v_mfma_f32_16x16x128_f8f6f4 v[154:157], v[2:9], v[194:201], v[154:157]
	v_mfma_f32_16x16x128_f8f6f4 v[142:145], v[10:17], v[214:221], v[142:145]
	v_mfma_f32_16x16x128_f8f6f4 v[138:141], v[2:9], v[214:221], v[138:141]
	v_mfma_f32_16x16x128_f8f6f4 v[126:129], v[10:17], v[222:229], v[126:129]
	v_mfma_f32_16x16x128_f8f6f4 v[122:125], v[2:9], v[222:229], v[122:125]
	v_mfma_f32_16x16x128_f8f6f4 v[102:105], v[10:17], v[230:237], v[102:105]
	v_mfma_f32_16x16x128_f8f6f4 v[98:101], v[2:9], v[230:237], v[98:101]
	s_setprio 0
	s_barrier
	s_add_u32 s28, s10, 0x180
	s_addc_u32 s29, s11, 0
	s_add_i32 s55, s55, s33
	ds_read_b128 v[194:197], v171 offset:49152
	ds_read_b128 v[198:201], v171 offset:50176
	ds_read_b128 v[214:217], v171 offset:51200
	ds_read_b128 v[218:221], v171 offset:52224
	ds_read_b128 v[222:225], v171 offset:53248
	ds_read_b128 v[226:229], v171 offset:54272
	ds_read_b128 v[230:233], v171 offset:55296
	ds_read_b128 v[234:237], v171 offset:56320
	s_mov_b32 m0, s55
	v_lshl_add_u64 v[186:187], s[28:29], 0, v[164:165]
	s_add_i32 s56, s55, 0x2000
	global_load_lds_dwordx4 v[186:187], off
	v_lshl_add_u64 v[186:187], s[28:29], 0, v[162:163]
	s_add_u32 s28, s10, 0x20180
	s_mov_b32 m0, s56
	s_addc_u32 s29, s11, 0
	s_add_i32 s57, s57, s33
	global_load_lds_dwordx4 v[186:187], off
	s_mov_b32 m0, s57
	v_lshl_add_u64 v[186:187], s[28:29], 0, v[164:165]
	s_add_i32 s58, s57, 0x2000
	global_load_lds_dwordx4 v[186:187], off
	v_lshl_add_u64 v[186:187], s[28:29], 0, v[162:163]
	s_mov_b32 m0, s58
	v_readlane_b32 s28, v254, 15
	global_load_lds_dwordx4 v[186:187], off
	v_readlane_b32 s29, v254, 16
	s_mov_b32 m0, s44
	s_nop 3
	global_load_lds_dwordx4 v170, s[28:29]
	s_mov_b32 m0, s45
	s_nop 0
	global_load_lds_dwordx4 v168, s[28:29]
	s_waitcnt vmcnt(8)
	s_waitcnt lgkmcnt(0)
	s_barrier
	s_setprio 1
	s_waitcnt lgkmcnt(0)
	v_mfma_f32_16x16x128_f8f6f4 v[94:97], v[26:33], v[194:201], v[94:97]
	v_mfma_f32_16x16x128_f8f6f4 v[86:89], v[18:25], v[194:201], v[86:89]
	v_mfma_f32_16x16x128_f8f6f4 v[70:73], v[26:33], v[214:221], v[70:73]
	v_mfma_f32_16x16x128_f8f6f4 v[66:69], v[18:25], v[214:221], v[66:69]
	v_mfma_f32_16x16x128_f8f6f4 v[54:57], v[26:33], v[222:229], v[54:57]
	v_mfma_f32_16x16x128_f8f6f4 v[50:53], v[18:25], v[222:229], v[50:53]
	v_mfma_f32_16x16x128_f8f6f4 v[38:41], v[26:33], v[230:237], v[38:41]
	v_mfma_f32_16x16x128_f8f6f4 v[34:37], v[18:25], v[230:237], v[34:37]
	s_setprio 0
	s_setprio 1
	v_mfma_f32_16x16x128_f8f6f4 v[110:113], v[10:17], v[194:201], v[110:113]
	v_mfma_f32_16x16x128_f8f6f4 v[106:109], v[2:9], v[194:201], v[106:109]
	v_mfma_f32_16x16x128_f8f6f4 v[78:81], v[10:17], v[214:221], v[78:81]
	v_mfma_f32_16x16x128_f8f6f4 v[74:77], v[2:9], v[214:221], v[74:77]
	v_mfma_f32_16x16x128_f8f6f4 v[62:65], v[10:17], v[222:229], v[62:65]
	v_mfma_f32_16x16x128_f8f6f4 v[58:61], v[2:9], v[222:229], v[58:61]
	v_mfma_f32_16x16x128_f8f6f4 v[46:49], v[10:17], v[230:237], v[46:49]
	v_mfma_f32_16x16x128_f8f6f4 v[42:45], v[2:9], v[230:237], v[42:45]
	s_setprio 0
	s_barrier
	s_mov_b32 s59, 0
	s_mov_b64 s[28:29], 0x1b300100

; #define PG8_STAGE(bufoff, gbase, voff) do { const char* gb_ = (const char*)(gbase); asm volatile("" : "+s"(gb_));     \
;         _Pragma("unroll") for (int _i = 0; _i < 2; ++_i) \
;         __builtin_amdgcn_global_load_lds((const unsigned*)(gb_ + (voff)[_i]), (LAS unsigned*)(lds + (bufoff) + ldsw + _i * 8192), 16, 0, 0); } while (0)
; #define PG8_STAGE_A(bufoff, gbase, h, vo) do { if constexpr (GATHER) { PG8_STAGE(bufoff, gbase, (vo)[h]); } else { PG8_STAGE(bufoff, (gbase) + (h) * hstep, voffA); } } while (0)
; #define PG8_WAIT_V(n) asm volatile("s_waitcnt vmcnt(" #n ")" ::: "memory")
; #define PG8_BAR __builtin_amdgcn_s_barrier()
;     ...
;     const int aoff = lds_byte(wr * 64 + fr, fq * 8), boff = lds_byte(wc * 32 + fr, fq * 8);
;     ...
;     if constexpr (SP2) {
;         PG8_STAGE(PG8_SB(0, 0), cB + PG8_KO(0), voffB); PG8_STAGE(PG8_SB(0, 1), cB + hstep + PG8_KO(0), voffB); PG8_STAGE_A(PG8_SA(0, 0), cA + PG8_KO(0), 0, cvo); PG8_STAGE_A(PG8_SA(0, 1), cA + PG8_KO(0), 1, cvo);
;         if (wr == 1) PG8_BAR;
;         PG8_WAIT_V(2); PG8_BAR;
;         PG8_STAGE(PG8_SB(1, 0), cB + PG8_KO(1), voffB); PG8_STAGE_A(PG8_SA(1, 0), cA + PG8_KO(1), 0, cvo); PG8_STAGE(PG8_SB(1, 1), cB + hstep + PG8_KO(1), voffB);
;         PG8_WAIT_V(6); PG8_BAR;
.LBB0_1489:
	s_lshl_b32 s6, s6, 5
	s_and_b32 s9, s6, 0x60
	s_lshl_b32 s8, s5, 13
	s_lshl_b32 s10, s9, 7
	s_add_u32 s6, s2, 0x80
	v_mov_b32_e32 v165, v191
	s_addc_u32 s7, s3, 0
	v_mov_b32_e32 v163, v191
	s_waitcnt vmcnt(2)
	s_barrier
	s_add_i32 m0, s44, 0x18000
	v_lshl_add_u64 v[4:5], s[6:7], 0, v[164:165]
	global_load_lds_dwordx4 v[4:5], off
	v_lshl_add_u64 v[4:5], s[6:7], 0, v[162:163]
	v_readlane_b32 s6, v254, 44
	s_add_i32 m0, s44, 0x1a000
	v_readlane_b32 s7, v254, 45
	s_add_i32 s50, s44, 0x8000
	global_load_lds_dwordx4 v[4:5], off
	s_mov_b32 m0, s50
	v_lshl_add_u64 v[4:5], s[6:7], 0, v[164:165]
	s_add_i32 s51, s44, 0xa000
	global_load_lds_dwordx4 v[4:5], off
	v_lshl_add_u64 v[4:5], s[6:7], 0, v[162:163]
	s_add_u32 s6, s2, 0x20080
	s_mov_b32 m0, s51
	s_addc_u32 s7, s3, 0
	global_load_lds_dwordx4 v[4:5], off
	s_add_i32 m0, s44, 0x1c000
	v_lshl_add_u64 v[4:5], s[6:7], 0, v[164:165]
	global_load_lds_dwordx4 v[4:5], off
	v_lshl_add_u64 v[4:5], s[6:7], 0, v[162:163]
	s_add_i32 m0, s44, 0x1e000
	v_readlane_b32 s6, v254, 36
	global_load_lds_dwordx4 v[4:5], off
	v_lshrrev_b32_e32 v4, 1, v2
	v_and_b32_e32 v4, 24, v4
	v_readlane_b32 s7, v254, 37
	v_and_b32_e32 v3, 15, v2
	v_lshlrev_b32_e32 v5, 1, v4
	v_lshlrev_b32_e32 v2, 2, v2
	s_mov_b32 s54, s6
	v_readlane_b32 s6, v254, 34
	v_lshl_or_b32 v1, s5, 6, v3
	v_lshl_or_b32 v3, v3, 6, v5
	v_and_b32_e32 v2, 32, v2
	s_waitcnt vmcnt(0)
	v_readlane_b32 s7, v254, 35
	v_bitop3_b32 v5, v3, s8, v2 bitop3:0xde
	s_cmpk_lt_u32 s4, 0x100
	s_mov_b32 s53, s6
	v_readlane_b32 s6, v254, 42
	v_bitop3_b32 v169, v3, s10, v2 bitop3:0xde
	s_cselect_b64 s[4:5], -1, 0
	v_or_b32_e32 v172, s9, v4
	s_mov_b32 s52, 0
	v_add_u32_e32 v173, 0, v5
	v_readlane_b32 s7, v254, 43
	s_barrier
	s_branch .LBB0_1492

.LBB0_1498:
	s_ashr_i32 s11, s10, 31
	s_lshl_b64 s[8:9], s[10:11], 18
	v_readlane_b32 s18, v252, 13
	v_readlane_b32 s19, v252, 14
	s_add_u32 s36, s18, s8
	s_addc_u32 s37, s19, s9
	s_ashr_i32 s35, s34, 31
	s_lshl_b64 s[8:9], s[34:35], 18
	s_add_u32 s38, s17, s8
	s_addc_u32 s39, s25, s9
	s_add_u32 s18, s6, 0x100
	s_addc_u32 s19, s7, 0
	s_add_u32 s28, s6, 0x180
	s_addc_u32 s29, s7, 0
	s_add_u32 s30, s2, 0x100
	s_addc_u32 s31, s3, 0
	s_add_i32 s55, 0, 0x10000
	s_add_i32 s57, 0, 0x14000
	v_add_u32_e32 v166, s55, v169
	v_add_u32_e32 v167, s57, v169
	ds_read_b128 v[2:5], v166
	ds_read_b128 v[6:9], v166 offset:1024
	ds_read_b128 v[10:13], v166 offset:2048
	ds_read_b128 v[14:17], v166 offset:3072
	ds_read_b128 v[18:21], v167
	ds_read_b128 v[22:25], v167 offset:1024
	ds_read_b128 v[26:29], v167 offset:2048
	ds_read_b128 v[30:33], v167 offset:3072
	s_mov_b64 s[8:9], 0x100
	s_add_u32 s40, s6, 0x20080
	s_addc_u32 s41, s7, 0
	s_add_i32 s11, s44, 0xc000
	ds_read_b128 v[34:37], v173
	ds_read_b128 v[38:41], v173 offset:1024
	ds_read_b128 v[42:45], v173 offset:2048
	ds_read_b128 v[46:49], v173 offset:3072
	ds_read_b128 v[50:53], v173 offset:4096
	ds_read_b128 v[54:57], v173 offset:5120
	ds_read_b128 v[58:61], v173 offset:6144
	ds_read_b128 v[62:65], v173 offset:7168
	s_mov_b32 m0, s11
	v_lshl_add_u64 v[66:67], s[40:41], 0, v[164:165]
	s_add_i32 s35, s44, 0xe000
	global_load_lds_dwordx4 v[66:67], off
	v_lshl_add_u64 v[66:67], s[40:41], 0, v[162:163]
	s_mov_b32 m0, s35
	s_nop 0
	global_load_lds_dwordx4 v[66:67], off
	s_waitcnt vmcnt(24)
	s_waitcnt lgkmcnt(0)
	s_barrier
	s_setprio 1
	s_waitcnt lgkmcnt(0)
	v_mfma_f32_16x16x128_f8f6f4 v[154:157], v[2:9], v[34:41], 0
	v_mfma_f32_16x16x128_f8f6f4 v[158:161], v[10:17], v[34:41], 0
	v_mfma_f32_16x16x128_f8f6f4 v[138:141], v[2:9], v[42:49], 0
	v_mfma_f32_16x16x128_f8f6f4 v[130:133], v[10:17], v[42:49], 0
	v_mfma_f32_16x16x128_f8f6f4 v[126:129], v[2:9], v[50:57], 0
	v_mfma_f32_16x16x128_f8f6f4 v[122:125], v[10:17], v[50:57], 0
	v_mfma_f32_16x16x128_f8f6f4 v[110:113], v[2:9], v[58:65], 0
	v_mfma_f32_16x16x128_f8f6f4 v[106:109], v[10:17], v[58:65], 0
	s_setprio 0
	s_setprio 1
	v_mfma_f32_16x16x128_f8f6f4 v[146:149], v[18:25], v[34:41], 0
	v_mfma_f32_16x16x128_f8f6f4 v[150:153], v[26:33], v[34:41], 0
	v_mfma_f32_16x16x128_f8f6f4 v[142:145], v[18:25], v[42:49], 0
	v_mfma_f32_16x16x128_f8f6f4 v[134:137], v[26:33], v[42:49], 0
	v_mfma_f32_16x16x128_f8f6f4 v[118:121], v[18:25], v[50:57], 0
	v_mfma_f32_16x16x128_f8f6f4 v[114:117], v[26:33], v[50:57], 0
	v_mfma_f32_16x16x128_f8f6f4 v[94:97], v[18:25], v[58:65], 0
	v_mfma_f32_16x16x128_f8f6f4 v[90:93], v[26:33], v[58:65], 0
	s_setprio 0
	s_barrier
	s_add_i32 s55, s55, s33
	ds_read_b128 v[34:37], v173 offset:16384
	ds_read_b128 v[38:41], v173 offset:17408
	ds_read_b128 v[50:53], v173 offset:18432
	ds_read_b128 v[54:57], v173 offset:19456
	ds_read_b128 v[174:177], v173 offset:20480
	ds_read_b128 v[178:181], v173 offset:21504
	ds_read_b128 v[182:185], v173 offset:22528
	ds_read_b128 v[186:189], v173 offset:23552
	s_mov_b32 m0, s55
	v_lshl_add_u64 v[42:43], s[30:31], 0, v[164:165]
	s_add_i32 s56, s55, 0x2000
	global_load_lds_dwordx4 v[42:43], off
	v_lshl_add_u64 v[42:43], s[30:31], 0, v[162:163]
	s_add_u32 s30, s2, 0x20100
	s_mov_b32 m0, s56
	s_addc_u32 s31, s3, 0
	s_add_i32 s57, s57, s33
	global_load_lds_dwordx4 v[42:43], off
	s_mov_b32 m0, s57
	v_lshl_add_u64 v[42:43], s[30:31], 0, v[164:165]
	s_add_i32 s58, s57, 0x2000
	global_load_lds_dwordx4 v[42:43], off
	v_lshl_add_u64 v[42:43], s[30:31], 0, v[162:163]
	s_mov_b32 m0, s58
	s_nop 0
	global_load_lds_dwordx4 v[42:43], off
	s_mov_b32 m0, s44
	v_lshl_add_u64 v[42:43], s[18:19], 0, v[164:165]
	global_load_lds_dwordx4 v[42:43], off
	v_lshl_add_u64 v[42:43], s[18:19], 0, v[162:163]
	s_mov_b32 m0, s45
	s_nop 0
	global_load_lds_dwordx4 v[42:43], off
	s_waitcnt vmcnt(24)
	s_waitcnt lgkmcnt(0)
	s_barrier
	s_setprio 1
	s_waitcnt lgkmcnt(0)
	v_mfma_f32_16x16x128_f8f6f4 v[102:105], v[2:9], v[34:41], 0
	v_mfma_f32_16x16x128_f8f6f4 v[98:101], v[10:17], v[34:41], 0
	v_mfma_f32_16x16x128_f8f6f4 v[78:81], v[2:9], v[50:57], 0
	v_mfma_f32_16x16x128_f8f6f4 v[74:77], v[10:17], v[50:57], 0
	v_mfma_f32_16x16x128_f8f6f4 v[62:65], v[2:9], v[174:181], 0
	v_mfma_f32_16x16x128_f8f6f4 v[58:61], v[10:17], v[174:181], 0
	v_mfma_f32_16x16x128_f8f6f4 v[46:49], v[2:9], v[182:189], 0
	v_mfma_f32_16x16x128_f8f6f4 v[42:45], v[10:17], v[182:189], 0
	s_setprio 0
	s_setprio 1
	v_mfma_f32_16x16x128_f8f6f4 v[86:89], v[18:25], v[34:41], 0
	v_mfma_f32_16x16x128_f8f6f4 v[82:85], v[26:33], v[34:41], 0
	v_mfma_f32_16x16x128_f8f6f4 v[70:73], v[18:25], v[50:57], 0
	v_mfma_f32_16x16x128_f8f6f4 v[66:69], v[26:33], v[50:57], 0
	v_mfma_f32_16x16x128_f8f6f4 v[54:57], v[18:25], v[174:181], 0
	v_mfma_f32_16x16x128_f8f6f4 v[50:53], v[26:33], v[174:181], 0
	v_mfma_f32_16x16x128_f8f6f4 v[38:41], v[18:25], v[182:189], 0
	v_mfma_f32_16x16x128_f8f6f4 v[34:37], v[26:33], v[182:189], 0
	s_setprio 0
	s_barrier
	s_add_i32 s40, 0, 0x18000
	s_add_i32 s59, 0, 0x1c000
	v_add_u32_e32 v168, s40, v169
	v_add_u32_e32 v170, s59, v169
	ds_read_b128 v[26:29], v168
	ds_read_b128 v[30:33], v168 offset:1024
	ds_read_b128 v[18:21], v168 offset:2048
	ds_read_b128 v[22:25], v168 offset:3072
	ds_read_b128 v[10:13], v170
	ds_read_b128 v[14:17], v170 offset:1024
	ds_read_b128 v[2:5], v170 offset:2048
	ds_read_b128 v[6:9], v170 offset:3072
	s_add_u32 s18, s6, 0x20100
	s_addc_u32 s19, s7, 0
	s_mov_b32 m0, s48
	ds_read_b128 v[174:177], v173 offset:32768
	ds_read_b128 v[178:181], v173 offset:33792
	ds_read_b128 v[182:185], v173 offset:34816
	ds_read_b128 v[186:189], v173 offset:35840
	ds_read_b128 v[194:197], v173 offset:36864
	ds_read_b128 v[198:201], v173 offset:37888
	ds_read_b128 v[214:217], v173 offset:38912
	ds_read_b128 v[218:221], v173 offset:39936
	s_nop 0
	v_lshl_add_u64 v[202:203], s[18:19], 0, v[164:165]
	global_load_lds_dwordx4 v[202:203], off
	v_lshl_add_u64 v[202:203], s[18:19], 0, v[162:163]
	s_mov_b32 m0, s49
	s_nop 0
	global_load_lds_dwordx4 v[202:203], off
	s_waitcnt vmcnt(8)
	s_waitcnt lgkmcnt(0)
	s_barrier
	s_setprio 1
	s_waitcnt lgkmcnt(0)
	v_mfma_f32_16x16x128_f8f6f4 v[154:157], v[26:33], v[174:181], v[154:157]
	v_mfma_f32_16x16x128_f8f6f4 v[158:161], v[18:25], v[174:181], v[158:161]
	v_mfma_f32_16x16x128_f8f6f4 v[138:141], v[26:33], v[182:189], v[138:141]
	v_mfma_f32_16x16x128_f8f6f4 v[130:133], v[18:25], v[182:189], v[130:133]
	v_mfma_f32_16x16x128_f8f6f4 v[126:129], v[26:33], v[194:201], v[126:129]
	v_mfma_f32_16x16x128_f8f6f4 v[122:125], v[18:25], v[194:201], v[122:125]
	v_mfma_f32_16x16x128_f8f6f4 v[110:113], v[26:33], v[214:221], v[110:113]
	v_mfma_f32_16x16x128_f8f6f4 v[106:109], v[18:25], v[214:221], v[106:109]
	s_setprio 0
	s_setprio 1
	v_mfma_f32_16x16x128_f8f6f4 v[146:149], v[10:17], v[174:181], v[146:149]
	v_mfma_f32_16x16x128_f8f6f4 v[150:153], v[2:9], v[174:181], v[150:153]
	v_mfma_f32_16x16x128_f8f6f4 v[142:145], v[10:17], v[182:189], v[142:145]
	v_mfma_f32_16x16x128_f8f6f4 v[134:137], v[2:9], v[182:189], v[134:137]
	v_mfma_f32_16x16x128_f8f6f4 v[118:121], v[10:17], v[194:201], v[118:121]
	v_mfma_f32_16x16x128_f8f6f4 v[114:117], v[2:9], v[194:201], v[114:117]
	v_mfma_f32_16x16x128_f8f6f4 v[94:97], v[10:17], v[214:221], v[94:97]
	v_mfma_f32_16x16x128_f8f6f4 v[90:93], v[2:9], v[214:221], v[90:93]
	s_setprio 0
	s_barrier
	s_add_u32 s30, s2, 0x180
	s_addc_u32 s31, s3, 0
	s_add_i32 s18, s40, s33
	ds_read_b128 v[174:177], v173 offset:49152
	ds_read_b128 v[178:181], v173 offset:50176
	ds_read_b128 v[182:185], v173 offset:51200
	ds_read_b128 v[186:189], v173 offset:52224
	ds_read_b128 v[194:197], v173 offset:53248
	ds_read_b128 v[198:201], v173 offset:54272
	ds_read_b128 v[214:217], v173 offset:55296
	ds_read_b128 v[218:221], v173 offset:56320
	s_mov_b32 m0, s18
	v_lshl_add_u64 v[202:203], s[30:31], 0, v[164:165]
	s_add_i32 s19, s18, 0x2000
	global_load_lds_dwordx4 v[202:203], off
	v_lshl_add_u64 v[202:203], s[30:31], 0, v[162:163]
	s_add_u32 s30, s2, 0x20180
	s_mov_b32 m0, s19
	s_addc_u32 s31, s3, 0
	s_add_i32 s59, s59, s33
	global_load_lds_dwordx4 v[202:203], off
	s_mov_b32 m0, s59
	v_lshl_add_u64 v[202:203], s[30:31], 0, v[164:165]
	s_add_i32 s60, s59, 0x2000
	global_load_lds_dwordx4 v[202:203], off
	v_lshl_add_u64 v[202:203], s[30:31], 0, v[162:163]
	s_mov_b32 m0, s60
	s_nop 0
	global_load_lds_dwordx4 v[202:203], off
	s_mov_b32 m0, s50
	v_lshl_add_u64 v[202:203], s[28:29], 0, v[164:165]
	global_load_lds_dwordx4 v[202:203], off
	v_lshl_add_u64 v[202:203], s[28:29], 0, v[162:163]
	s_mov_b32 m0, s51
	s_nop 0
	global_load_lds_dwordx4 v[202:203], off
	s_waitcnt vmcnt(8)
	s_waitcnt lgkmcnt(0)
	s_barrier
	s_setprio 1
	s_waitcnt lgkmcnt(0)
	v_mfma_f32_16x16x128_f8f6f4 v[102:105], v[26:33], v[174:181], v[102:105]
	v_mfma_f32_16x16x128_f8f6f4 v[98:101], v[18:25], v[174:181], v[98:101]
	v_mfma_f32_16x16x128_f8f6f4 v[78:81], v[26:33], v[182:189], v[78:81]
	v_mfma_f32_16x16x128_f8f6f4 v[74:77], v[18:25], v[182:189], v[74:77]
	v_mfma_f32_16x16x128_f8f6f4 v[62:65], v[26:33], v[194:201], v[62:65]
	v_mfma_f32_16x16x128_f8f6f4 v[58:61], v[18:25], v[194:201], v[58:61]
	v_mfma_f32_16x16x128_f8f6f4 v[46:49], v[26:33], v[214:221], v[46:49]
	v_mfma_f32_16x16x128_f8f6f4 v[42:45], v[18:25], v[214:221], v[42:45]
	s_setprio 0
	s_setprio 1
	v_mfma_f32_16x16x128_f8f6f4 v[86:89], v[10:17], v[174:181], v[86:89]
	v_mfma_f32_16x16x128_f8f6f4 v[82:85], v[2:9], v[174:181], v[82:85]
	v_mfma_f32_16x16x128_f8f6f4 v[70:73], v[10:17], v[182:189], v[70:73]
	v_mfma_f32_16x16x128_f8f6f4 v[66:69], v[2:9], v[182:189], v[66:69]
	v_mfma_f32_16x16x128_f8f6f4 v[54:57], v[10:17], v[194:201], v[54:57]
	v_mfma_f32_16x16x128_f8f6f4 v[50:53], v[2:9], v[194:201], v[50:53]
	v_mfma_f32_16x16x128_f8f6f4 v[38:41], v[10:17], v[214:221], v[38:41]
	v_mfma_f32_16x16x128_f8f6f4 v[34:37], v[2:9], v[214:221], v[34:37]
	s_setprio 0
	s_barrier
	s_mov_b32 s61, 0
